# DSA top-k scoring: 120 LDS key tiles software-pipelined in interleaved pairs (double-buffered fragments, scalar group skips), redundant NaN-canonicalize ops dropped
# speedup vs baseline: 1.0264x; 1.0004x over previous
.LBB0_586:
	s_or_b64 exec, exec, s[0:1]
	s_waitcnt vmcnt(7)
	v_mfma_f32_16x16x32_bf16 v[40:43], v[8:11], v[40:43], 0
	v_lshlrev_b32_e32 v76, 16, v78
	v_and_b32_e32 v77, 0xffff0000, v78
	v_and_b32_e32 v78, 0xffff0000, v79
	s_waitcnt vmcnt(6)
	v_mfma_f32_16x16x32_bf16 v[36:39], v[8:11], v[36:39], 0
	v_lshlrev_b32_e32 v79, 16, v79
	s_nop 1
	v_max_f32_e32 v42, v42, v42
	v_max_f32_e32 v133, 0, v42
	v_max_f32_e32 v42, v43, v43
	v_max_f32_e32 v40, v40, v40
	v_max_f32_e32 v41, v41, v41
	v_max_f32_e32 v132, 0, v42
	v_max_f32_e32 v36, v36, v36
	v_max_f32_e32 v37, v37, v37
	v_max_f32_e32 v38, v38, v38
	v_max_f32_e32 v40, 0, v40
	v_max_f32_e32 v41, 0, v41
	v_pk_mul_f32 v[42:43], v[132:133], v[78:79]
	v_max_f32_e32 v36, 0, v36
	v_max_f32_e32 v37, 0, v37
	v_max_f32_e32 v133, 0, v38
	v_max_f32_e32 v38, v39, v39
	v_pk_mul_f32 v[40:41], v[40:41], v[76:77]
	v_pk_mul_f32 v[36:37], v[36:37], v[76:77]
	v_max_f32_e32 v132, 0, v38
	v_pk_mul_f32 v[38:39], v[132:133], v[78:79]
	v_mov_b32_e32 v132, v36
	v_mov_b32_e32 v133, v40
	v_mov_b32_e32 v40, v37
	v_pk_add_f32 v[36:37], v[132:133], v[40:41]
	v_mov_b32_e32 v40, v39
	v_mov_b32_e32 v41, v43
	v_pk_add_f32 v[36:37], v[40:41], v[36:37]
	v_mov_b32_e32 v39, v42
	v_pk_add_f32 v[36:37], v[38:39], v[36:37]
	s_waitcnt vmcnt(5)
	v_mfma_f32_16x16x32_bf16 v[32:35], v[8:11], v[32:35], 0
	v_add_f32_e64 v36, v36, 0
	v_add_f32_e64 v37, v37, 0
	v_mov_b32_e32 v210, 0
	v_min_u32_e32 v39, -2, v37
	v_or_b32_e32 v38, 0x80000000, v37
	v_not_b32_e32 v39, v39
	v_cmp_gt_i32_e32 vcc, 0, v37
	v_min_u32_e32 v40, -2, v36
	v_not_b32_e32 v40, v40
	v_cndmask_b32_e32 v38, v38, v39, vcc
	v_or_b32_e32 v39, 0x80000000, v36
	v_cmp_gt_i32_e64 s[0:1], 0, v36
	v_or_b32_e32 v36, 16, v89
	s_waitcnt vmcnt(4)
	v_mfma_f32_16x16x32_bf16 v[28:31], v[8:11], v[28:31], 0
	v_cndmask_b32_e64 v39, v39, v40, s[0:1]
	v_cmp_gt_i32_e64 s[0:1], v36, v72
	v_cmp_gt_i32_e32 vcc, v89, v72
	v_max_f32_e32 v34, v34, v34
	v_cndmask_b32_e64 v36, v39, 0, s[0:1]
	v_min_u32_e32 v39, v38, v39
	v_cndmask_b32_e64 v37, v38, 0, vcc
	v_cndmask_b32_e64 v38, v39, v38, s[0:1]
	v_max_f32_e32 v39, 0, v34
	v_max_f32_e32 v34, v35, v35
	v_cndmask_b32_e64 v41, v38, -1, vcc
	v_max_f32_e32 v32, v32, v32
	v_max_f32_e32 v33, v33, v33
	v_max_f32_e32 v38, 0, v34
	v_max_f32_e32 v28, v28, v28
	v_max_f32_e32 v29, v29, v29
	v_max_f32_e32 v30, v30, v30
	v_max_f32_e32 v32, 0, v32
	v_max_f32_e32 v33, 0, v33
	v_pk_mul_f32 v[34:35], v[38:39], v[78:79]
	v_max_f32_e32 v28, 0, v28
	v_max_f32_e32 v29, 0, v29
	v_max_f32_e32 v39, 0, v30
	v_max_f32_e32 v30, v31, v31
	v_pk_mul_f32 v[32:33], v[32:33], v[76:77]
	v_pk_mul_f32 v[28:29], v[28:29], v[76:77]
	v_max_f32_e32 v38, 0, v30
	v_pk_mul_f32 v[30:31], v[38:39], v[78:79]
	v_mov_b32_e32 v38, v28
	v_mov_b32_e32 v39, v32
	v_mov_b32_e32 v32, v29
	v_pk_add_f32 v[28:29], v[38:39], v[32:33]
	v_mov_b32_e32 v32, v31
	v_mov_b32_e32 v33, v35
	v_pk_add_f32 v[28:29], v[32:33], v[28:29]
	v_mov_b32_e32 v31, v34
	v_pk_add_f32 v[28:29], v[30:31], v[28:29]
	s_waitcnt vmcnt(3)
	v_mfma_f32_16x16x32_bf16 v[24:27], v[8:11], v[24:27], 0
	v_add_f32_e64 v28, v28, 0
	v_add_f32_e64 v29, v29, 0
	v_max_u32_e32 v40, v37, v36
	v_min_u32_e32 v31, -2, v29
	v_or_b32_e32 v30, 0x80000000, v29
	v_not_b32_e32 v31, v31
	v_cmp_gt_i32_e32 vcc, 0, v29
	v_or_b32_e32 v29, 32, v89
	v_min_u32_e32 v32, -2, v28
	v_cndmask_b32_e32 v30, v30, v31, vcc
	v_cmp_gt_i32_e32 vcc, v29, v72
	v_or_b32_e32 v31, 0x80000000, v28
	v_not_b32_e32 v32, v32
	v_cndmask_b32_e64 v29, v30, 0, vcc
	v_min_u32_e32 v30, v41, v30
	v_cndmask_b32_e32 v30, v30, v41, vcc
	v_cmp_gt_i32_e32 vcc, 0, v28
	v_or_b32_e32 v28, 48, v89
	s_waitcnt vmcnt(2)
	v_mfma_f32_16x16x32_bf16 v[20:23], v[8:11], v[20:23], 0
	v_cndmask_b32_e32 v31, v31, v32, vcc
	v_cmp_gt_i32_e32 vcc, v28, v72
	v_max_f32_e32 v26, v26, v26
	v_max_f32_e32 v24, v24, v24
	v_cndmask_b32_e64 v28, v31, 0, vcc
	v_min_u32_e32 v31, v30, v31
	v_cndmask_b32_e32 v33, v31, v30, vcc
	v_max_f32_e32 v31, 0, v26
	v_max_f32_e32 v26, v27, v27
	v_max_f32_e32 v25, v25, v25
	v_max_f32_e32 v30, 0, v26
	v_max_f32_e32 v20, v20, v20
	v_max_f32_e32 v21, v21, v21
	v_max_f32_e32 v22, v22, v22
	v_max_f32_e32 v24, 0, v24
	v_max_f32_e32 v25, 0, v25
	v_pk_mul_f32 v[26:27], v[30:31], v[78:79]
	v_max_f32_e32 v20, 0, v20
	v_max_f32_e32 v21, 0, v21
	v_max_f32_e32 v31, 0, v22
	v_max_f32_e32 v22, v23, v23
	v_pk_mul_f32 v[24:25], v[24:25], v[76:77]
	v_pk_mul_f32 v[20:21], v[20:21], v[76:77]
	v_max_f32_e32 v30, 0, v22
	v_pk_mul_f32 v[22:23], v[30:31], v[78:79]
	v_mov_b32_e32 v30, v20
	v_mov_b32_e32 v31, v24
	v_mov_b32_e32 v24, v21
	v_pk_add_f32 v[20:21], v[30:31], v[24:25]
	v_mov_b32_e32 v24, v23
	v_mov_b32_e32 v25, v27
	v_pk_add_f32 v[20:21], v[24:25], v[20:21]
	v_mov_b32_e32 v23, v26
	v_pk_add_f32 v[20:21], v[22:23], v[20:21]
	s_waitcnt vmcnt(1)
	v_mfma_f32_16x16x32_bf16 v[16:19], v[8:11], v[16:19], 0
	v_add_f32_e64 v20, v20, 0
	v_add_f32_e64 v21, v21, 0
	v_max3_u32 v32, v40, v29, v28
	v_min_u32_e32 v23, -2, v21
	v_or_b32_e32 v22, 0x80000000, v21
	v_not_b32_e32 v23, v23
	v_cmp_gt_i32_e32 vcc, 0, v21
	v_or_b32_e32 v21, 64, v89
	v_min_u32_e32 v24, -2, v20
	v_cndmask_b32_e32 v22, v22, v23, vcc
	v_cmp_gt_i32_e32 vcc, v21, v72
	v_or_b32_e32 v23, 0x80000000, v20
	v_not_b32_e32 v24, v24
	v_cndmask_b32_e64 v21, v22, 0, vcc
	v_min_u32_e32 v22, v33, v22
	v_cndmask_b32_e32 v22, v22, v33, vcc
	v_cmp_gt_i32_e32 vcc, 0, v20
	v_or_b32_e32 v20, 0x50, v89
	s_waitcnt vmcnt(0)
	v_mfma_f32_16x16x32_bf16 v[12:15], v[8:11], v[12:15], 0
	v_cndmask_b32_e32 v23, v23, v24, vcc
	v_cmp_gt_i32_e32 vcc, v20, v72
	v_max_f32_e32 v18, v18, v18
	v_max_f32_e32 v16, v16, v16
	v_cndmask_b32_e64 v20, v23, 0, vcc
	v_min_u32_e32 v23, v22, v23
	v_cndmask_b32_e32 v25, v23, v22, vcc
	v_max_f32_e32 v23, 0, v18
	v_max_f32_e32 v18, v19, v19
	v_max_f32_e32 v17, v17, v17
	v_max_f32_e32 v22, 0, v18
	v_max_f32_e32 v12, v12, v12
	v_max_f32_e32 v13, v13, v13
	v_max_f32_e32 v14, v14, v14
	v_max_f32_e32 v16, 0, v16
	v_max_f32_e32 v17, 0, v17
	v_pk_mul_f32 v[18:19], v[22:23], v[78:79]
	v_max_f32_e32 v12, 0, v12
	v_max_f32_e32 v13, 0, v13
	v_max_f32_e32 v23, 0, v14
	v_max_f32_e32 v14, v15, v15
	v_pk_mul_f32 v[16:17], v[16:17], v[76:77]
	v_pk_mul_f32 v[12:13], v[12:13], v[76:77]
	v_max_f32_e32 v22, 0, v14
	v_pk_mul_f32 v[14:15], v[22:23], v[78:79]
	v_mov_b32_e32 v22, v12
	v_mov_b32_e32 v23, v16
	v_mov_b32_e32 v16, v13
	v_pk_add_f32 v[12:13], v[22:23], v[16:17]
	v_mov_b32_e32 v16, v15
	v_mov_b32_e32 v17, v19
	v_pk_add_f32 v[12:13], v[16:17], v[12:13]
	v_mov_b32_e32 v15, v18
	v_pk_add_f32 v[12:13], v[14:15], v[12:13]
	v_max3_u32 v24, v32, v21, v20
	v_pk_add_f32 v[12:13], v[12:13], 0 op_sel_hi:[1,0]
	v_mov_b32_e32 v247, 0
	v_min_u32_e32 v15, -2, v13
	v_or_b32_e32 v14, 0x80000000, v13
	v_not_b32_e32 v15, v15
	v_cmp_gt_i32_e32 vcc, 0, v13
	s_nop 1
	v_cndmask_b32_e32 v13, v14, v15, vcc
	v_or_b32_e32 v14, 0x60, v89
	v_cmp_gt_i32_e32 vcc, v14, v72
	v_min_u32_e32 v14, -2, v12
	v_not_b32_e32 v14, v14
	v_cndmask_b32_e64 v15, v13, 0, vcc
	v_min_u32_e32 v13, v25, v13
	v_cndmask_b32_e32 v16, v13, v25, vcc
	v_or_b32_e32 v13, 0x80000000, v12
	v_cmp_gt_i32_e32 vcc, 0, v12
	s_nop 1
	v_cndmask_b32_e32 v12, v13, v14, vcc
	v_or_b32_e32 v13, 0x70, v89
	v_cmp_gt_i32_e32 vcc, v13, v72
	s_nop 1
	v_cndmask_b32_e64 v14, v12, 0, vcc
	v_min_u32_e32 v12, v16, v12
	v_max3_u32 v13, v24, v15, v14
	v_cndmask_b32_e32 v12, v12, v16, vcc
	s_cmp_eq_u64 s[16:17], 0
	s_cbranch_scc1 .Lmy_sel_zero_0
	v_add_u32_e32 v215, 0x10000, v87
	ds_read_b128 v[248:251], v87
	ds_read_b128 v[222:225], v87 offset:1024
	s_waitcnt lgkmcnt(0)
	v_mfma_f32_16x16x32_bf16 v[248:251], v[8:11], v[248:251], 0
	v_mfma_f32_16x16x32_bf16 v[222:225], v[8:11], v[222:225], 0
	s_nop 5
	ds_read_b128 v[16:19], v87 offset:2048
	ds_read_b128 v[24:27], v87 offset:3072
	v_max_f32_e32 v248, 0, v248
	v_max_f32_e32 v222, 0, v222
	v_max_f32_e32 v249, 0, v249
	v_max_f32_e32 v223, 0, v223
	v_max_f32_e32 v250, 0, v250
	v_max_f32_e32 v224, 0, v224
	v_max_f32_e32 v251, 0, v251
	v_max_f32_e32 v225, 0, v225
	v_pk_mul_f32 v[248:249], v[248:249], v[76:77]
	v_pk_mul_f32 v[222:223], v[222:223], v[76:77]
	v_mul_f32_e32 v250, v79, v250
	v_mul_f32_e32 v224, v79, v224
	v_mul_f32_e32 v251, v78, v251
	v_mul_f32_e32 v225, v78, v225
	v_add_f32_e32 v248, v248, v249
	v_add_f32_e32 v222, v222, v223
	v_add_f32_e32 v248, v250, v248
	v_add_f32_e32 v222, v224, v222
	v_add_f32_e32 v248, v251, v248
	v_add_f32_e32 v222, v225, v222
	v_add_f32_e32 v248, 0, v248
	v_add_f32_e32 v222, 0, v222
	v_min_u32_e32 v250, -2, v248
	v_min_u32_e32 v224, -2, v222
	v_or_b32_e32 v249, 0x80000000, v248
	v_or_b32_e32 v223, 0x80000000, v222
	v_not_b32_e32 v250, v250
	v_not_b32_e32 v224, v224
	v_cmp_gt_i32_e32 vcc, 0, v248
	v_cmp_gt_i32_e64 s[0:1], 0, v222
	s_waitcnt lgkmcnt(0)
	v_mfma_f32_16x16x32_bf16 v[16:19], v[8:11], v[16:19], 0
	v_mfma_f32_16x16x32_bf16 v[24:27], v[8:11], v[24:27], 0
	v_cndmask_b32_e32 v247, v249, v250, vcc
	v_cndmask_b32_e64 v246, v223, v224, s[0:1]
	v_max_u32_e32 v13, v13, v247
	v_min_u32_e32 v12, v12, v247
	v_max_u32_e32 v13, v13, v246
	v_min_u32_e32 v12, v12, v246
	ds_read_b128 v[248:251], v87 offset:4096
	ds_read_b128 v[222:225], v87 offset:5120
	v_max_f32_e32 v16, 0, v16
	v_max_f32_e32 v24, 0, v24
	v_max_f32_e32 v17, 0, v17
	v_max_f32_e32 v25, 0, v25
	v_max_f32_e32 v18, 0, v18
	v_max_f32_e32 v26, 0, v26
	v_max_f32_e32 v19, 0, v19
	v_max_f32_e32 v27, 0, v27
	v_pk_mul_f32 v[16:17], v[16:17], v[76:77]
	v_pk_mul_f32 v[24:25], v[24:25], v[76:77]
	v_mul_f32_e32 v18, v79, v18
	v_mul_f32_e32 v26, v79, v26
	v_mul_f32_e32 v19, v78, v19
	v_mul_f32_e32 v27, v78, v27
	v_add_f32_e32 v16, v16, v17
	v_add_f32_e32 v24, v24, v25
	v_add_f32_e32 v16, v18, v16
	v_add_f32_e32 v24, v26, v24
	v_add_f32_e32 v16, v19, v16
	v_add_f32_e32 v24, v27, v24
	v_add_f32_e32 v16, 0, v16
	v_add_f32_e32 v24, 0, v24
	v_min_u32_e32 v18, -2, v16
	v_min_u32_e32 v26, -2, v24
	v_or_b32_e32 v17, 0x80000000, v16
	v_or_b32_e32 v25, 0x80000000, v24
	v_not_b32_e32 v18, v18
	v_not_b32_e32 v26, v26
	v_cmp_gt_i32_e32 vcc, 0, v16
	v_cmp_gt_i32_e64 s[0:1], 0, v24
	s_waitcnt lgkmcnt(0)
	v_mfma_f32_16x16x32_bf16 v[248:251], v[8:11], v[248:251], 0
	v_mfma_f32_16x16x32_bf16 v[222:225], v[8:11], v[222:225], 0
	v_cndmask_b32_e32 v210, v17, v18, vcc
	v_cndmask_b32_e64 v245, v25, v26, s[0:1]
	v_max_u32_e32 v13, v13, v210
	v_min_u32_e32 v12, v12, v210
	v_max_u32_e32 v13, v13, v245
	v_min_u32_e32 v12, v12, v245
	ds_read_b128 v[16:19], v87 offset:6144
	ds_read_b128 v[24:27], v87 offset:7168
	v_max_f32_e32 v248, 0, v248
	v_max_f32_e32 v222, 0, v222
	v_max_f32_e32 v249, 0, v249
	v_max_f32_e32 v223, 0, v223
	v_max_f32_e32 v250, 0, v250
	v_max_f32_e32 v224, 0, v224
	v_max_f32_e32 v251, 0, v251
	v_max_f32_e32 v225, 0, v225
	v_pk_mul_f32 v[248:249], v[248:249], v[76:77]
	v_pk_mul_f32 v[222:223], v[222:223], v[76:77]
	v_mul_f32_e32 v250, v79, v250
	v_mul_f32_e32 v224, v79, v224
	v_mul_f32_e32 v251, v78, v251
	v_mul_f32_e32 v225, v78, v225
	v_add_f32_e32 v248, v248, v249
	v_add_f32_e32 v222, v222, v223
	v_add_f32_e32 v248, v250, v248
	v_add_f32_e32 v222, v224, v222
	v_add_f32_e32 v248, v251, v248
	v_add_f32_e32 v222, v225, v222
	v_add_f32_e32 v248, 0, v248
	v_add_f32_e32 v222, 0, v222
	v_min_u32_e32 v250, -2, v248
	v_min_u32_e32 v224, -2, v222
	v_or_b32_e32 v249, 0x80000000, v248
	v_or_b32_e32 v223, 0x80000000, v222
	v_not_b32_e32 v250, v250
	v_not_b32_e32 v224, v224
	v_cmp_gt_i32_e32 vcc, 0, v248
	v_cmp_gt_i32_e64 s[0:1], 0, v222
	s_waitcnt lgkmcnt(0)
	v_mfma_f32_16x16x32_bf16 v[16:19], v[8:11], v[16:19], 0
	v_mfma_f32_16x16x32_bf16 v[24:27], v[8:11], v[24:27], 0
	v_cndmask_b32_e32 v239, v249, v250, vcc
	v_cndmask_b32_e64 v244, v223, v224, s[0:1]
	v_max_u32_e32 v13, v13, v239
	v_min_u32_e32 v12, v12, v239
	v_max_u32_e32 v13, v13, v244
	v_min_u32_e32 v12, v12, v244
	ds_read_b128 v[248:251], v87 offset:8192
	ds_read_b128 v[222:225], v87 offset:9216
	v_max_f32_e32 v16, 0, v16
	v_max_f32_e32 v24, 0, v24
	v_max_f32_e32 v17, 0, v17
	v_max_f32_e32 v25, 0, v25
	v_max_f32_e32 v18, 0, v18
	v_max_f32_e32 v26, 0, v26
	v_max_f32_e32 v19, 0, v19
	v_max_f32_e32 v27, 0, v27
	v_pk_mul_f32 v[16:17], v[16:17], v[76:77]
	v_pk_mul_f32 v[24:25], v[24:25], v[76:77]
	v_mul_f32_e32 v18, v79, v18
	v_mul_f32_e32 v26, v79, v26
	v_mul_f32_e32 v19, v78, v19
	v_mul_f32_e32 v27, v78, v27
	v_add_f32_e32 v16, v16, v17
	v_add_f32_e32 v24, v24, v25
	v_add_f32_e32 v16, v18, v16
	v_add_f32_e32 v24, v26, v24
	v_add_f32_e32 v16, v19, v16
	v_add_f32_e32 v24, v27, v24
	v_add_f32_e32 v16, 0, v16
	v_add_f32_e32 v24, 0, v24
	v_min_u32_e32 v18, -2, v16
	v_min_u32_e32 v26, -2, v24
	v_or_b32_e32 v17, 0x80000000, v16
	v_or_b32_e32 v25, 0x80000000, v24
	v_not_b32_e32 v18, v18
	v_not_b32_e32 v26, v26
	v_cmp_gt_i32_e32 vcc, 0, v16
	v_cmp_gt_i32_e64 s[0:1], 0, v24
	s_waitcnt lgkmcnt(0)
	v_mfma_f32_16x16x32_bf16 v[248:251], v[8:11], v[248:251], 0
	v_mfma_f32_16x16x32_bf16 v[222:225], v[8:11], v[222:225], 0
	v_cndmask_b32_e32 v237, v17, v18, vcc
	v_cndmask_b32_e64 v243, v25, v26, s[0:1]
	v_max_u32_e32 v13, v13, v237
	v_min_u32_e32 v12, v12, v237
	v_max_u32_e32 v13, v13, v243
	v_min_u32_e32 v12, v12, v243
	s_cmp_eq_u64 s[18:19], 0
	s_cbranch_scc1 .Lmy_sel_zero_1
	ds_read_b128 v[16:19], v87 offset:10240
	ds_read_b128 v[24:27], v87 offset:11264
	v_max_f32_e32 v248, 0, v248
	v_max_f32_e32 v222, 0, v222
	v_max_f32_e32 v249, 0, v249
	v_max_f32_e32 v223, 0, v223
	v_max_f32_e32 v250, 0, v250
	v_max_f32_e32 v224, 0, v224
	v_max_f32_e32 v251, 0, v251
	v_max_f32_e32 v225, 0, v225
	v_pk_mul_f32 v[248:249], v[248:249], v[76:77]
	v_pk_mul_f32 v[222:223], v[222:223], v[76:77]
	v_mul_f32_e32 v250, v79, v250
	v_mul_f32_e32 v224, v79, v224
	v_mul_f32_e32 v251, v78, v251
	v_mul_f32_e32 v225, v78, v225
	v_add_f32_e32 v248, v248, v249
	v_add_f32_e32 v222, v222, v223
	v_add_f32_e32 v248, v250, v248
	v_add_f32_e32 v222, v224, v222
	v_add_f32_e32 v248, v251, v248
	v_add_f32_e32 v222, v225, v222
	v_add_f32_e32 v248, 0, v248
	v_add_f32_e32 v222, 0, v222
	v_min_u32_e32 v250, -2, v248
	v_min_u32_e32 v224, -2, v222
	v_or_b32_e32 v249, 0x80000000, v248
	v_or_b32_e32 v223, 0x80000000, v222
	v_not_b32_e32 v250, v250
	v_not_b32_e32 v224, v224
	v_cmp_gt_i32_e32 vcc, 0, v248
	v_cmp_gt_i32_e64 s[0:1], 0, v222
	s_waitcnt lgkmcnt(0)
	v_mfma_f32_16x16x32_bf16 v[16:19], v[8:11], v[16:19], 0
	v_mfma_f32_16x16x32_bf16 v[24:27], v[8:11], v[24:27], 0
	v_cndmask_b32_e32 v235, v249, v250, vcc
	v_cndmask_b32_e64 v242, v223, v224, s[0:1]
	v_max_u32_e32 v13, v13, v235
	v_min_u32_e32 v12, v12, v235
	v_max_u32_e32 v13, v13, v242
	v_min_u32_e32 v12, v12, v242
	ds_read_b128 v[248:251], v87 offset:12288
	ds_read_b128 v[222:225], v87 offset:13312
	v_max_f32_e32 v16, 0, v16
	v_max_f32_e32 v24, 0, v24
	v_max_f32_e32 v17, 0, v17
	v_max_f32_e32 v25, 0, v25
	v_max_f32_e32 v18, 0, v18
	v_max_f32_e32 v26, 0, v26
	v_max_f32_e32 v19, 0, v19
	v_max_f32_e32 v27, 0, v27
	v_pk_mul_f32 v[16:17], v[16:17], v[76:77]
	v_pk_mul_f32 v[24:25], v[24:25], v[76:77]
	v_mul_f32_e32 v18, v79, v18
	v_mul_f32_e32 v26, v79, v26
	v_mul_f32_e32 v19, v78, v19
	v_mul_f32_e32 v27, v78, v27
	v_add_f32_e32 v16, v16, v17
	v_add_f32_e32 v24, v24, v25
	v_add_f32_e32 v16, v18, v16
	v_add_f32_e32 v24, v26, v24
	v_add_f32_e32 v16, v19, v16
	v_add_f32_e32 v24, v27, v24
	v_add_f32_e32 v16, 0, v16
	v_add_f32_e32 v24, 0, v24
	v_min_u32_e32 v18, -2, v16
	v_min_u32_e32 v26, -2, v24
	v_or_b32_e32 v17, 0x80000000, v16
	v_or_b32_e32 v25, 0x80000000, v24
	v_not_b32_e32 v18, v18
	v_not_b32_e32 v26, v26
	v_cmp_gt_i32_e32 vcc, 0, v16
	v_cmp_gt_i32_e64 s[0:1], 0, v24
	s_waitcnt lgkmcnt(0)
	v_mfma_f32_16x16x32_bf16 v[248:251], v[8:11], v[248:251], 0
	v_mfma_f32_16x16x32_bf16 v[222:225], v[8:11], v[222:225], 0
	v_cndmask_b32_e32 v212, v17, v18, vcc
	v_cndmask_b32_e64 v241, v25, v26, s[0:1]
	v_max_u32_e32 v13, v13, v212
	v_min_u32_e32 v12, v12, v212
	v_max_u32_e32 v13, v13, v241
	v_min_u32_e32 v12, v12, v241
	ds_read_b128 v[16:19], v87 offset:14336
	ds_read_b128 v[24:27], v87 offset:15360
	v_max_f32_e32 v248, 0, v248
	v_max_f32_e32 v222, 0, v222
	v_max_f32_e32 v249, 0, v249
	v_max_f32_e32 v223, 0, v223
	v_max_f32_e32 v250, 0, v250
	v_max_f32_e32 v224, 0, v224
	v_max_f32_e32 v251, 0, v251
	v_max_f32_e32 v225, 0, v225
	v_pk_mul_f32 v[248:249], v[248:249], v[76:77]
	v_pk_mul_f32 v[222:223], v[222:223], v[76:77]
	v_mul_f32_e32 v250, v79, v250
	v_mul_f32_e32 v224, v79, v224
	v_mul_f32_e32 v251, v78, v251
	v_mul_f32_e32 v225, v78, v225
	v_add_f32_e32 v248, v248, v249
	v_add_f32_e32 v222, v222, v223
	v_add_f32_e32 v248, v250, v248
	v_add_f32_e32 v222, v224, v222
	v_add_f32_e32 v248, v251, v248
	v_add_f32_e32 v222, v225, v222
	v_add_f32_e32 v248, 0, v248
	v_add_f32_e32 v222, 0, v222
	v_min_u32_e32 v250, -2, v248
	v_min_u32_e32 v224, -2, v222
	v_or_b32_e32 v249, 0x80000000, v248
	v_or_b32_e32 v223, 0x80000000, v222
	v_not_b32_e32 v250, v250
	v_not_b32_e32 v224, v224
	v_cmp_gt_i32_e32 vcc, 0, v248
	v_cmp_gt_i32_e64 s[0:1], 0, v222
	s_waitcnt lgkmcnt(0)
	v_mfma_f32_16x16x32_bf16 v[16:19], v[8:11], v[16:19], 0
	v_mfma_f32_16x16x32_bf16 v[24:27], v[8:11], v[24:27], 0
	v_cndmask_b32_e32 v209, v249, v250, vcc
	v_cndmask_b32_e64 v240, v223, v224, s[0:1]
	v_max_u32_e32 v13, v13, v209
	v_min_u32_e32 v12, v12, v209
	v_max_u32_e32 v13, v13, v240
	v_min_u32_e32 v12, v12, v240
	ds_read_b128 v[248:251], v87 offset:16384
	ds_read_b128 v[222:225], v87 offset:17408
	v_max_f32_e32 v16, 0, v16
	v_max_f32_e32 v24, 0, v24
	v_max_f32_e32 v17, 0, v17
	v_max_f32_e32 v25, 0, v25
	v_max_f32_e32 v18, 0, v18
	v_max_f32_e32 v26, 0, v26
	v_max_f32_e32 v19, 0, v19
	v_max_f32_e32 v27, 0, v27
	v_pk_mul_f32 v[16:17], v[16:17], v[76:77]
	v_pk_mul_f32 v[24:25], v[24:25], v[76:77]
	v_mul_f32_e32 v18, v79, v18
	v_mul_f32_e32 v26, v79, v26
	v_mul_f32_e32 v19, v78, v19
	v_mul_f32_e32 v27, v78, v27
	v_add_f32_e32 v16, v16, v17
	v_add_f32_e32 v24, v24, v25
	v_add_f32_e32 v16, v18, v16
	v_add_f32_e32 v24, v26, v24
	v_add_f32_e32 v16, v19, v16
	v_add_f32_e32 v24, v27, v24
	v_add_f32_e32 v16, 0, v16
	v_add_f32_e32 v24, 0, v24
	v_min_u32_e32 v18, -2, v16
	v_min_u32_e32 v26, -2, v24
	v_or_b32_e32 v17, 0x80000000, v16
	v_or_b32_e32 v25, 0x80000000, v24
	v_not_b32_e32 v18, v18
	v_not_b32_e32 v26, v26
	v_cmp_gt_i32_e32 vcc, 0, v16
	v_cmp_gt_i32_e64 s[0:1], 0, v24
	s_waitcnt lgkmcnt(0)
	v_mfma_f32_16x16x32_bf16 v[248:251], v[8:11], v[248:251], 0
	v_mfma_f32_16x16x32_bf16 v[222:225], v[8:11], v[222:225], 0
	v_cndmask_b32_e32 v207, v17, v18, vcc
	v_cndmask_b32_e64 v238, v25, v26, s[0:1]
	v_max_u32_e32 v13, v13, v207
	v_min_u32_e32 v12, v12, v207
	v_max_u32_e32 v13, v13, v238
	v_min_u32_e32 v12, v12, v238
	s_cmp_eq_u64 s[20:21], 0
	s_cbranch_scc1 .Lmy_sel_zero_2
	ds_read_b128 v[16:19], v87 offset:18432
	ds_read_b128 v[24:27], v87 offset:19456
	v_max_f32_e32 v248, 0, v248
	v_max_f32_e32 v222, 0, v222
	v_max_f32_e32 v249, 0, v249
	v_max_f32_e32 v223, 0, v223
	v_max_f32_e32 v250, 0, v250
	v_max_f32_e32 v224, 0, v224
	v_max_f32_e32 v251, 0, v251
	v_max_f32_e32 v225, 0, v225
	v_pk_mul_f32 v[248:249], v[248:249], v[76:77]
	v_pk_mul_f32 v[222:223], v[222:223], v[76:77]
	v_mul_f32_e32 v250, v79, v250
	v_mul_f32_e32 v224, v79, v224
	v_mul_f32_e32 v251, v78, v251
	v_mul_f32_e32 v225, v78, v225
	v_add_f32_e32 v248, v248, v249
	v_add_f32_e32 v222, v222, v223
	v_add_f32_e32 v248, v250, v248
	v_add_f32_e32 v222, v224, v222
	v_add_f32_e32 v248, v251, v248
	v_add_f32_e32 v222, v225, v222
	v_add_f32_e32 v248, 0, v248
	v_add_f32_e32 v222, 0, v222
	v_min_u32_e32 v250, -2, v248
	v_min_u32_e32 v224, -2, v222
	v_or_b32_e32 v249, 0x80000000, v248
	v_or_b32_e32 v223, 0x80000000, v222
	v_not_b32_e32 v250, v250
	v_not_b32_e32 v224, v224
	v_cmp_gt_i32_e32 vcc, 0, v248
	v_cmp_gt_i32_e64 s[0:1], 0, v222
	s_waitcnt lgkmcnt(0)
	v_mfma_f32_16x16x32_bf16 v[16:19], v[8:11], v[16:19], 0
	v_mfma_f32_16x16x32_bf16 v[24:27], v[8:11], v[24:27], 0
	v_cndmask_b32_e32 v205, v249, v250, vcc
	v_cndmask_b32_e64 v236, v223, v224, s[0:1]
	v_max_u32_e32 v13, v13, v205
	v_min_u32_e32 v12, v12, v205
	v_max_u32_e32 v13, v13, v236
	v_min_u32_e32 v12, v12, v236
	ds_read_b128 v[248:251], v87 offset:20480
	ds_read_b128 v[222:225], v87 offset:21504
	v_max_f32_e32 v16, 0, v16
	v_max_f32_e32 v24, 0, v24
	v_max_f32_e32 v17, 0, v17
	v_max_f32_e32 v25, 0, v25
	v_max_f32_e32 v18, 0, v18
	v_max_f32_e32 v26, 0, v26
	v_max_f32_e32 v19, 0, v19
	v_max_f32_e32 v27, 0, v27
	v_pk_mul_f32 v[16:17], v[16:17], v[76:77]
	v_pk_mul_f32 v[24:25], v[24:25], v[76:77]
	v_mul_f32_e32 v18, v79, v18
	v_mul_f32_e32 v26, v79, v26
	v_mul_f32_e32 v19, v78, v19
	v_mul_f32_e32 v27, v78, v27
	v_add_f32_e32 v16, v16, v17
	v_add_f32_e32 v24, v24, v25
	v_add_f32_e32 v16, v18, v16
	v_add_f32_e32 v24, v26, v24
	v_add_f32_e32 v16, v19, v16
	v_add_f32_e32 v24, v27, v24
	v_add_f32_e32 v16, 0, v16
	v_add_f32_e32 v24, 0, v24
	v_min_u32_e32 v18, -2, v16
	v_min_u32_e32 v26, -2, v24
	v_or_b32_e32 v17, 0x80000000, v16
	v_or_b32_e32 v25, 0x80000000, v24
	v_not_b32_e32 v18, v18
	v_not_b32_e32 v26, v26
	v_cmp_gt_i32_e32 vcc, 0, v16
	v_cmp_gt_i32_e64 s[0:1], 0, v24
	s_waitcnt lgkmcnt(0)
	v_mfma_f32_16x16x32_bf16 v[248:251], v[8:11], v[248:251], 0
	v_mfma_f32_16x16x32_bf16 v[222:225], v[8:11], v[222:225], 0
	v_cndmask_b32_e32 v203, v17, v18, vcc
	v_cndmask_b32_e64 v213, v25, v26, s[0:1]
	v_max_u32_e32 v13, v13, v203
	v_min_u32_e32 v12, v12, v203
	v_max_u32_e32 v13, v13, v213
	v_min_u32_e32 v12, v12, v213
	ds_read_b128 v[16:19], v87 offset:22528
	ds_read_b128 v[24:27], v87 offset:23552
	v_max_f32_e32 v248, 0, v248
	v_max_f32_e32 v222, 0, v222
	v_max_f32_e32 v249, 0, v249
	v_max_f32_e32 v223, 0, v223
	v_max_f32_e32 v250, 0, v250
	v_max_f32_e32 v224, 0, v224
	v_max_f32_e32 v251, 0, v251
	v_max_f32_e32 v225, 0, v225
	v_pk_mul_f32 v[248:249], v[248:249], v[76:77]
	v_pk_mul_f32 v[222:223], v[222:223], v[76:77]
	v_mul_f32_e32 v250, v79, v250
	v_mul_f32_e32 v224, v79, v224
	v_mul_f32_e32 v251, v78, v251
	v_mul_f32_e32 v225, v78, v225
	v_add_f32_e32 v248, v248, v249
	v_add_f32_e32 v222, v222, v223
	v_add_f32_e32 v248, v250, v248
	v_add_f32_e32 v222, v224, v222
	v_add_f32_e32 v248, v251, v248
	v_add_f32_e32 v222, v225, v222
	v_add_f32_e32 v248, 0, v248
	v_add_f32_e32 v222, 0, v222
	v_min_u32_e32 v250, -2, v248
	v_min_u32_e32 v224, -2, v222
	v_or_b32_e32 v249, 0x80000000, v248
	v_or_b32_e32 v223, 0x80000000, v222
	v_not_b32_e32 v250, v250
	v_not_b32_e32 v224, v224
	v_cmp_gt_i32_e32 vcc, 0, v248
	v_cmp_gt_i32_e64 s[0:1], 0, v222
	s_waitcnt lgkmcnt(0)
	v_mfma_f32_16x16x32_bf16 v[16:19], v[8:11], v[16:19], 0
	v_mfma_f32_16x16x32_bf16 v[24:27], v[8:11], v[24:27], 0
	v_cndmask_b32_e32 v201, v249, v250, vcc
	v_cndmask_b32_e64 v211, v223, v224, s[0:1]
	v_max_u32_e32 v13, v13, v201
	v_min_u32_e32 v12, v12, v201
	v_max_u32_e32 v13, v13, v211
	v_min_u32_e32 v12, v12, v211
	ds_read_b128 v[248:251], v87 offset:24576
	ds_read_b128 v[222:225], v87 offset:25600
	v_max_f32_e32 v16, 0, v16
	v_max_f32_e32 v24, 0, v24
	v_max_f32_e32 v17, 0, v17
	v_max_f32_e32 v25, 0, v25
	v_max_f32_e32 v18, 0, v18
	v_max_f32_e32 v26, 0, v26
	v_max_f32_e32 v19, 0, v19
	v_max_f32_e32 v27, 0, v27
	v_pk_mul_f32 v[16:17], v[16:17], v[76:77]
	v_pk_mul_f32 v[24:25], v[24:25], v[76:77]
	v_mul_f32_e32 v18, v79, v18
	v_mul_f32_e32 v26, v79, v26
	v_mul_f32_e32 v19, v78, v19
	v_mul_f32_e32 v27, v78, v27
	v_add_f32_e32 v16, v16, v17
	v_add_f32_e32 v24, v24, v25
	v_add_f32_e32 v16, v18, v16
	v_add_f32_e32 v24, v26, v24
	v_add_f32_e32 v16, v19, v16
	v_add_f32_e32 v24, v27, v24
	v_add_f32_e32 v16, 0, v16
	v_add_f32_e32 v24, 0, v24
	v_min_u32_e32 v18, -2, v16
	v_min_u32_e32 v26, -2, v24
	v_or_b32_e32 v17, 0x80000000, v16
	v_or_b32_e32 v25, 0x80000000, v24
	v_not_b32_e32 v18, v18
	v_not_b32_e32 v26, v26
	v_cmp_gt_i32_e32 vcc, 0, v16
	v_cmp_gt_i32_e64 s[0:1], 0, v24
	s_waitcnt lgkmcnt(0)
	v_mfma_f32_16x16x32_bf16 v[248:251], v[8:11], v[248:251], 0
	v_mfma_f32_16x16x32_bf16 v[222:225], v[8:11], v[222:225], 0
	v_cndmask_b32_e32 v199, v17, v18, vcc
	v_cndmask_b32_e64 v208, v25, v26, s[0:1]
	v_max_u32_e32 v13, v13, v199
	v_min_u32_e32 v12, v12, v199
	v_max_u32_e32 v13, v13, v208
	v_min_u32_e32 v12, v12, v208
	s_cmp_eq_u64 s[8:9], 0
	s_cbranch_scc1 .Lmy_sel_zero_3
	ds_read_b128 v[16:19], v87 offset:26624
	ds_read_b128 v[24:27], v87 offset:27648
	v_max_f32_e32 v248, 0, v248
	v_max_f32_e32 v222, 0, v222
	v_max_f32_e32 v249, 0, v249
	v_max_f32_e32 v223, 0, v223
	v_max_f32_e32 v250, 0, v250
	v_max_f32_e32 v224, 0, v224
	v_max_f32_e32 v251, 0, v251
	v_max_f32_e32 v225, 0, v225
	v_pk_mul_f32 v[248:249], v[248:249], v[76:77]
	v_pk_mul_f32 v[222:223], v[222:223], v[76:77]
	v_mul_f32_e32 v250, v79, v250
	v_mul_f32_e32 v224, v79, v224
	v_mul_f32_e32 v251, v78, v251
	v_mul_f32_e32 v225, v78, v225
	v_add_f32_e32 v248, v248, v249
	v_add_f32_e32 v222, v222, v223
	v_add_f32_e32 v248, v250, v248
	v_add_f32_e32 v222, v224, v222
	v_add_f32_e32 v248, v251, v248
	v_add_f32_e32 v222, v225, v222
	v_add_f32_e32 v248, 0, v248
	v_add_f32_e32 v222, 0, v222
	v_min_u32_e32 v250, -2, v248
	v_min_u32_e32 v224, -2, v222
	v_or_b32_e32 v249, 0x80000000, v248
	v_or_b32_e32 v223, 0x80000000, v222
	v_not_b32_e32 v250, v250
	v_not_b32_e32 v224, v224
	v_cmp_gt_i32_e32 vcc, 0, v248
	v_cmp_gt_i32_e64 s[0:1], 0, v222
	s_waitcnt lgkmcnt(0)
	v_mfma_f32_16x16x32_bf16 v[16:19], v[8:11], v[16:19], 0
	v_mfma_f32_16x16x32_bf16 v[24:27], v[8:11], v[24:27], 0
	v_cndmask_b32_e32 v197, v249, v250, vcc
	v_cndmask_b32_e64 v206, v223, v224, s[0:1]
	v_max_u32_e32 v13, v13, v197
	v_min_u32_e32 v12, v12, v197
	v_max_u32_e32 v13, v13, v206
	v_min_u32_e32 v12, v12, v206
	ds_read_b128 v[248:251], v87 offset:28672
	ds_read_b128 v[222:225], v87 offset:29696
	v_max_f32_e32 v16, 0, v16
	v_max_f32_e32 v24, 0, v24
	v_max_f32_e32 v17, 0, v17
	v_max_f32_e32 v25, 0, v25
	v_max_f32_e32 v18, 0, v18
	v_max_f32_e32 v26, 0, v26
	v_max_f32_e32 v19, 0, v19
	v_max_f32_e32 v27, 0, v27
	v_pk_mul_f32 v[16:17], v[16:17], v[76:77]
	v_pk_mul_f32 v[24:25], v[24:25], v[76:77]
	v_mul_f32_e32 v18, v79, v18
	v_mul_f32_e32 v26, v79, v26
	v_mul_f32_e32 v19, v78, v19
	v_mul_f32_e32 v27, v78, v27
	v_add_f32_e32 v16, v16, v17
	v_add_f32_e32 v24, v24, v25
	v_add_f32_e32 v16, v18, v16
	v_add_f32_e32 v24, v26, v24
	v_add_f32_e32 v16, v19, v16
	v_add_f32_e32 v24, v27, v24
	v_add_f32_e32 v16, 0, v16
	v_add_f32_e32 v24, 0, v24
	v_min_u32_e32 v18, -2, v16
	v_min_u32_e32 v26, -2, v24
	v_or_b32_e32 v17, 0x80000000, v16
	v_or_b32_e32 v25, 0x80000000, v24
	v_not_b32_e32 v18, v18
	v_not_b32_e32 v26, v26
	v_cmp_gt_i32_e32 vcc, 0, v16
	v_cmp_gt_i32_e64 s[0:1], 0, v24
	s_waitcnt lgkmcnt(0)
	v_mfma_f32_16x16x32_bf16 v[248:251], v[8:11], v[248:251], 0
	v_mfma_f32_16x16x32_bf16 v[222:225], v[8:11], v[222:225], 0
	v_cndmask_b32_e32 v195, v17, v18, vcc
	v_cndmask_b32_e64 v204, v25, v26, s[0:1]
	v_max_u32_e32 v13, v13, v195
	v_min_u32_e32 v12, v12, v195
	v_max_u32_e32 v13, v13, v204
	v_min_u32_e32 v12, v12, v204
	ds_read_b128 v[16:19], v87 offset:30720
	ds_read_b128 v[24:27], v87 offset:31744
	v_max_f32_e32 v248, 0, v248
	v_max_f32_e32 v222, 0, v222
	v_max_f32_e32 v249, 0, v249
	v_max_f32_e32 v223, 0, v223
	v_max_f32_e32 v250, 0, v250
	v_max_f32_e32 v224, 0, v224
	v_max_f32_e32 v251, 0, v251
	v_max_f32_e32 v225, 0, v225
	v_pk_mul_f32 v[248:249], v[248:249], v[76:77]
	v_pk_mul_f32 v[222:223], v[222:223], v[76:77]
	v_mul_f32_e32 v250, v79, v250
	v_mul_f32_e32 v224, v79, v224
	v_mul_f32_e32 v251, v78, v251
	v_mul_f32_e32 v225, v78, v225
	v_add_f32_e32 v248, v248, v249
	v_add_f32_e32 v222, v222, v223
	v_add_f32_e32 v248, v250, v248
	v_add_f32_e32 v222, v224, v222
	v_add_f32_e32 v248, v251, v248
	v_add_f32_e32 v222, v225, v222
	v_add_f32_e32 v248, 0, v248
	v_add_f32_e32 v222, 0, v222
	v_min_u32_e32 v250, -2, v248
	v_min_u32_e32 v224, -2, v222
	v_or_b32_e32 v249, 0x80000000, v248
	v_or_b32_e32 v223, 0x80000000, v222
	v_not_b32_e32 v250, v250
	v_not_b32_e32 v224, v224
	v_cmp_gt_i32_e32 vcc, 0, v248
	v_cmp_gt_i32_e64 s[0:1], 0, v222
	s_waitcnt lgkmcnt(0)
	v_mfma_f32_16x16x32_bf16 v[16:19], v[8:11], v[16:19], 0
	v_mfma_f32_16x16x32_bf16 v[24:27], v[8:11], v[24:27], 0
	v_cndmask_b32_e32 v193, v249, v250, vcc
	v_cndmask_b32_e64 v202, v223, v224, s[0:1]
	v_max_u32_e32 v13, v13, v193
	v_min_u32_e32 v12, v12, v193
	v_max_u32_e32 v13, v13, v202
	v_min_u32_e32 v12, v12, v202
	ds_read_b128 v[248:251], v87 offset:32768
	ds_read_b128 v[222:225], v87 offset:33792
	v_max_f32_e32 v16, 0, v16
	v_max_f32_e32 v24, 0, v24
	v_max_f32_e32 v17, 0, v17
	v_max_f32_e32 v25, 0, v25
	v_max_f32_e32 v18, 0, v18
	v_max_f32_e32 v26, 0, v26
	v_max_f32_e32 v19, 0, v19
	v_max_f32_e32 v27, 0, v27
	v_pk_mul_f32 v[16:17], v[16:17], v[76:77]
	v_pk_mul_f32 v[24:25], v[24:25], v[76:77]
	v_mul_f32_e32 v18, v79, v18
	v_mul_f32_e32 v26, v79, v26
	v_mul_f32_e32 v19, v78, v19
	v_mul_f32_e32 v27, v78, v27
	v_add_f32_e32 v16, v16, v17
	v_add_f32_e32 v24, v24, v25
	v_add_f32_e32 v16, v18, v16
	v_add_f32_e32 v24, v26, v24
	v_add_f32_e32 v16, v19, v16
	v_add_f32_e32 v24, v27, v24
	v_add_f32_e32 v16, 0, v16
	v_add_f32_e32 v24, 0, v24
	v_min_u32_e32 v18, -2, v16
	v_min_u32_e32 v26, -2, v24
	v_or_b32_e32 v17, 0x80000000, v16
	v_or_b32_e32 v25, 0x80000000, v24
	v_not_b32_e32 v18, v18
	v_not_b32_e32 v26, v26
	v_cmp_gt_i32_e32 vcc, 0, v16
	v_cmp_gt_i32_e64 s[0:1], 0, v24
	s_waitcnt lgkmcnt(0)
	v_mfma_f32_16x16x32_bf16 v[248:251], v[8:11], v[248:251], 0
	v_mfma_f32_16x16x32_bf16 v[222:225], v[8:11], v[222:225], 0
	v_cndmask_b32_e32 v191, v17, v18, vcc
	v_cndmask_b32_e64 v200, v25, v26, s[0:1]
	v_max_u32_e32 v13, v13, v191
	v_min_u32_e32 v12, v12, v191
	v_max_u32_e32 v13, v13, v200
	v_min_u32_e32 v12, v12, v200
	s_cmp_eq_u64 s[22:23], 0
	s_cbranch_scc1 .Lmy_sel_zero_4
	ds_read_b128 v[16:19], v87 offset:34816
	ds_read_b128 v[24:27], v87 offset:35840
	v_max_f32_e32 v248, 0, v248
	v_max_f32_e32 v222, 0, v222
	v_max_f32_e32 v249, 0, v249
	v_max_f32_e32 v223, 0, v223
	v_max_f32_e32 v250, 0, v250
	v_max_f32_e32 v224, 0, v224
	v_max_f32_e32 v251, 0, v251
	v_max_f32_e32 v225, 0, v225
	v_pk_mul_f32 v[248:249], v[248:249], v[76:77]
	v_pk_mul_f32 v[222:223], v[222:223], v[76:77]
	v_mul_f32_e32 v250, v79, v250
	v_mul_f32_e32 v224, v79, v224
	v_mul_f32_e32 v251, v78, v251
	v_mul_f32_e32 v225, v78, v225
	v_add_f32_e32 v248, v248, v249
	v_add_f32_e32 v222, v222, v223
	v_add_f32_e32 v248, v250, v248
	v_add_f32_e32 v222, v224, v222
	v_add_f32_e32 v248, v251, v248
	v_add_f32_e32 v222, v225, v222
	v_add_f32_e32 v248, 0, v248
	v_add_f32_e32 v222, 0, v222
	v_min_u32_e32 v250, -2, v248
	v_min_u32_e32 v224, -2, v222
	v_or_b32_e32 v249, 0x80000000, v248
	v_or_b32_e32 v223, 0x80000000, v222
	v_not_b32_e32 v250, v250
	v_not_b32_e32 v224, v224
	v_cmp_gt_i32_e32 vcc, 0, v248
	v_cmp_gt_i32_e64 s[0:1], 0, v222
	s_waitcnt lgkmcnt(0)
	v_mfma_f32_16x16x32_bf16 v[16:19], v[8:11], v[16:19], 0
	v_mfma_f32_16x16x32_bf16 v[24:27], v[8:11], v[24:27], 0
	v_cndmask_b32_e32 v189, v249, v250, vcc
	v_cndmask_b32_e64 v198, v223, v224, s[0:1]
	v_max_u32_e32 v13, v13, v189
	v_min_u32_e32 v12, v12, v189
	v_max_u32_e32 v13, v13, v198
	v_min_u32_e32 v12, v12, v198
	ds_read_b128 v[248:251], v87 offset:36864
	ds_read_b128 v[222:225], v87 offset:37888
	v_max_f32_e32 v16, 0, v16
	v_max_f32_e32 v24, 0, v24
	v_max_f32_e32 v17, 0, v17
	v_max_f32_e32 v25, 0, v25
	v_max_f32_e32 v18, 0, v18
	v_max_f32_e32 v26, 0, v26
	v_max_f32_e32 v19, 0, v19
	v_max_f32_e32 v27, 0, v27
	v_pk_mul_f32 v[16:17], v[16:17], v[76:77]
	v_pk_mul_f32 v[24:25], v[24:25], v[76:77]
	v_mul_f32_e32 v18, v79, v18
	v_mul_f32_e32 v26, v79, v26
	v_mul_f32_e32 v19, v78, v19
	v_mul_f32_e32 v27, v78, v27
	v_add_f32_e32 v16, v16, v17
	v_add_f32_e32 v24, v24, v25
	v_add_f32_e32 v16, v18, v16
	v_add_f32_e32 v24, v26, v24
	v_add_f32_e32 v16, v19, v16
	v_add_f32_e32 v24, v27, v24
	v_add_f32_e32 v16, 0, v16
	v_add_f32_e32 v24, 0, v24
	v_min_u32_e32 v18, -2, v16
	v_min_u32_e32 v26, -2, v24
	v_or_b32_e32 v17, 0x80000000, v16
	v_or_b32_e32 v25, 0x80000000, v24
	v_not_b32_e32 v18, v18
	v_not_b32_e32 v26, v26
	v_cmp_gt_i32_e32 vcc, 0, v16
	v_cmp_gt_i32_e64 s[0:1], 0, v24
	s_waitcnt lgkmcnt(0)
	v_mfma_f32_16x16x32_bf16 v[248:251], v[8:11], v[248:251], 0
	v_mfma_f32_16x16x32_bf16 v[222:225], v[8:11], v[222:225], 0
	v_cndmask_b32_e32 v187, v17, v18, vcc
	v_cndmask_b32_e64 v196, v25, v26, s[0:1]
	v_max_u32_e32 v13, v13, v187
	v_min_u32_e32 v12, v12, v187
	v_max_u32_e32 v13, v13, v196
	v_min_u32_e32 v12, v12, v196
	ds_read_b128 v[16:19], v87 offset:38912
	ds_read_b128 v[24:27], v87 offset:39936
	v_max_f32_e32 v248, 0, v248
	v_max_f32_e32 v222, 0, v222
	v_max_f32_e32 v249, 0, v249
	v_max_f32_e32 v223, 0, v223
	v_max_f32_e32 v250, 0, v250
	v_max_f32_e32 v224, 0, v224
	v_max_f32_e32 v251, 0, v251
	v_max_f32_e32 v225, 0, v225
	v_pk_mul_f32 v[248:249], v[248:249], v[76:77]
	v_pk_mul_f32 v[222:223], v[222:223], v[76:77]
	v_mul_f32_e32 v250, v79, v250
	v_mul_f32_e32 v224, v79, v224
	v_mul_f32_e32 v251, v78, v251
	v_mul_f32_e32 v225, v78, v225
	v_add_f32_e32 v248, v248, v249
	v_add_f32_e32 v222, v222, v223
	v_add_f32_e32 v248, v250, v248
	v_add_f32_e32 v222, v224, v222
	v_add_f32_e32 v248, v251, v248
	v_add_f32_e32 v222, v225, v222
	v_add_f32_e32 v248, 0, v248
	v_add_f32_e32 v222, 0, v222
	v_min_u32_e32 v250, -2, v248
	v_min_u32_e32 v224, -2, v222
	v_or_b32_e32 v249, 0x80000000, v248
	v_or_b32_e32 v223, 0x80000000, v222
	v_not_b32_e32 v250, v250
	v_not_b32_e32 v224, v224
	v_cmp_gt_i32_e32 vcc, 0, v248
	v_cmp_gt_i32_e64 s[0:1], 0, v222
	s_waitcnt lgkmcnt(0)
	v_mfma_f32_16x16x32_bf16 v[16:19], v[8:11], v[16:19], 0
	v_mfma_f32_16x16x32_bf16 v[24:27], v[8:11], v[24:27], 0
	v_cndmask_b32_e32 v185, v249, v250, vcc
	v_cndmask_b32_e64 v194, v223, v224, s[0:1]
	v_max_u32_e32 v13, v13, v185
	v_min_u32_e32 v12, v12, v185
	v_max_u32_e32 v13, v13, v194
	v_min_u32_e32 v12, v12, v194
	ds_read_b128 v[248:251], v87 offset:40960
	ds_read_b128 v[222:225], v87 offset:41984
	v_max_f32_e32 v16, 0, v16
	v_max_f32_e32 v24, 0, v24
	v_max_f32_e32 v17, 0, v17
	v_max_f32_e32 v25, 0, v25
	v_max_f32_e32 v18, 0, v18
	v_max_f32_e32 v26, 0, v26
	v_max_f32_e32 v19, 0, v19
	v_max_f32_e32 v27, 0, v27
	v_pk_mul_f32 v[16:17], v[16:17], v[76:77]
	v_pk_mul_f32 v[24:25], v[24:25], v[76:77]
	v_mul_f32_e32 v18, v79, v18
	v_mul_f32_e32 v26, v79, v26
	v_mul_f32_e32 v19, v78, v19
	v_mul_f32_e32 v27, v78, v27
	v_add_f32_e32 v16, v16, v17
	v_add_f32_e32 v24, v24, v25
	v_add_f32_e32 v16, v18, v16
	v_add_f32_e32 v24, v26, v24
	v_add_f32_e32 v16, v19, v16
	v_add_f32_e32 v24, v27, v24
	v_add_f32_e32 v16, 0, v16
	v_add_f32_e32 v24, 0, v24
	v_min_u32_e32 v18, -2, v16
	v_min_u32_e32 v26, -2, v24
	v_or_b32_e32 v17, 0x80000000, v16
	v_or_b32_e32 v25, 0x80000000, v24
	v_not_b32_e32 v18, v18
	v_not_b32_e32 v26, v26
	v_cmp_gt_i32_e32 vcc, 0, v16
	v_cmp_gt_i32_e64 s[0:1], 0, v24
	s_waitcnt lgkmcnt(0)
	v_mfma_f32_16x16x32_bf16 v[248:251], v[8:11], v[248:251], 0
	v_mfma_f32_16x16x32_bf16 v[222:225], v[8:11], v[222:225], 0
	v_cndmask_b32_e32 v183, v17, v18, vcc
	v_cndmask_b32_e64 v192, v25, v26, s[0:1]
	v_max_u32_e32 v13, v13, v183
	v_min_u32_e32 v12, v12, v183
	v_max_u32_e32 v13, v13, v192
	v_min_u32_e32 v12, v12, v192
	s_cmp_eq_u64 s[24:25], 0
	s_cbranch_scc1 .Lmy_sel_zero_5
	ds_read_b128 v[16:19], v87 offset:43008
	ds_read_b128 v[24:27], v87 offset:44032
	v_max_f32_e32 v248, 0, v248
	v_max_f32_e32 v222, 0, v222
	v_max_f32_e32 v249, 0, v249
	v_max_f32_e32 v223, 0, v223
	v_max_f32_e32 v250, 0, v250
	v_max_f32_e32 v224, 0, v224
	v_max_f32_e32 v251, 0, v251
	v_max_f32_e32 v225, 0, v225
	v_pk_mul_f32 v[248:249], v[248:249], v[76:77]
	v_pk_mul_f32 v[222:223], v[222:223], v[76:77]
	v_mul_f32_e32 v250, v79, v250
	v_mul_f32_e32 v224, v79, v224
	v_mul_f32_e32 v251, v78, v251
	v_mul_f32_e32 v225, v78, v225
	v_add_f32_e32 v248, v248, v249
	v_add_f32_e32 v222, v222, v223
	v_add_f32_e32 v248, v250, v248
	v_add_f32_e32 v222, v224, v222
	v_add_f32_e32 v248, v251, v248
	v_add_f32_e32 v222, v225, v222
	v_add_f32_e32 v248, 0, v248
	v_add_f32_e32 v222, 0, v222
	v_min_u32_e32 v250, -2, v248
	v_min_u32_e32 v224, -2, v222
	v_or_b32_e32 v249, 0x80000000, v248
	v_or_b32_e32 v223, 0x80000000, v222
	v_not_b32_e32 v250, v250
	v_not_b32_e32 v224, v224
	v_cmp_gt_i32_e32 vcc, 0, v248
	v_cmp_gt_i32_e64 s[0:1], 0, v222
	s_waitcnt lgkmcnt(0)
	v_mfma_f32_16x16x32_bf16 v[16:19], v[8:11], v[16:19], 0
	v_mfma_f32_16x16x32_bf16 v[24:27], v[8:11], v[24:27], 0
	v_cndmask_b32_e32 v181, v249, v250, vcc
	v_cndmask_b32_e64 v190, v223, v224, s[0:1]
	v_max_u32_e32 v13, v13, v181
	v_min_u32_e32 v12, v12, v181
	v_max_u32_e32 v13, v13, v190
	v_min_u32_e32 v12, v12, v190
	ds_read_b128 v[248:251], v87 offset:45056
	ds_read_b128 v[222:225], v87 offset:46080
	v_max_f32_e32 v16, 0, v16
	v_max_f32_e32 v24, 0, v24
	v_max_f32_e32 v17, 0, v17
	v_max_f32_e32 v25, 0, v25
	v_max_f32_e32 v18, 0, v18
	v_max_f32_e32 v26, 0, v26
	v_max_f32_e32 v19, 0, v19
	v_max_f32_e32 v27, 0, v27
	v_pk_mul_f32 v[16:17], v[16:17], v[76:77]
	v_pk_mul_f32 v[24:25], v[24:25], v[76:77]
	v_mul_f32_e32 v18, v79, v18
	v_mul_f32_e32 v26, v79, v26
	v_mul_f32_e32 v19, v78, v19
	v_mul_f32_e32 v27, v78, v27
	v_add_f32_e32 v16, v16, v17
	v_add_f32_e32 v24, v24, v25
	v_add_f32_e32 v16, v18, v16
	v_add_f32_e32 v24, v26, v24
	v_add_f32_e32 v16, v19, v16
	v_add_f32_e32 v24, v27, v24
	v_add_f32_e32 v16, 0, v16
	v_add_f32_e32 v24, 0, v24
	v_min_u32_e32 v18, -2, v16
	v_min_u32_e32 v26, -2, v24
	v_or_b32_e32 v17, 0x80000000, v16
	v_or_b32_e32 v25, 0x80000000, v24
	v_not_b32_e32 v18, v18
	v_not_b32_e32 v26, v26
	v_cmp_gt_i32_e32 vcc, 0, v16
	v_cmp_gt_i32_e64 s[0:1], 0, v24
	s_waitcnt lgkmcnt(0)
	v_mfma_f32_16x16x32_bf16 v[248:251], v[8:11], v[248:251], 0
	v_mfma_f32_16x16x32_bf16 v[222:225], v[8:11], v[222:225], 0
	v_cndmask_b32_e32 v179, v17, v18, vcc
	v_cndmask_b32_e64 v188, v25, v26, s[0:1]
	v_max_u32_e32 v13, v13, v179
	v_min_u32_e32 v12, v12, v179
	v_max_u32_e32 v13, v13, v188
	v_min_u32_e32 v12, v12, v188
	ds_read_b128 v[16:19], v87 offset:47104
	ds_read_b128 v[24:27], v87 offset:48128
	v_max_f32_e32 v248, 0, v248
	v_max_f32_e32 v222, 0, v222
	v_max_f32_e32 v249, 0, v249
	v_max_f32_e32 v223, 0, v223
	v_max_f32_e32 v250, 0, v250
	v_max_f32_e32 v224, 0, v224
	v_max_f32_e32 v251, 0, v251
	v_max_f32_e32 v225, 0, v225
	v_pk_mul_f32 v[248:249], v[248:249], v[76:77]
	v_pk_mul_f32 v[222:223], v[222:223], v[76:77]
	v_mul_f32_e32 v250, v79, v250
	v_mul_f32_e32 v224, v79, v224
	v_mul_f32_e32 v251, v78, v251
	v_mul_f32_e32 v225, v78, v225
	v_add_f32_e32 v248, v248, v249
	v_add_f32_e32 v222, v222, v223
	v_add_f32_e32 v248, v250, v248
	v_add_f32_e32 v222, v224, v222
	v_add_f32_e32 v248, v251, v248
	v_add_f32_e32 v222, v225, v222
	v_add_f32_e32 v248, 0, v248
	v_add_f32_e32 v222, 0, v222
	v_min_u32_e32 v250, -2, v248
	v_min_u32_e32 v224, -2, v222
	v_or_b32_e32 v249, 0x80000000, v248
	v_or_b32_e32 v223, 0x80000000, v222
	v_not_b32_e32 v250, v250
	v_not_b32_e32 v224, v224
	v_cmp_gt_i32_e32 vcc, 0, v248
	v_cmp_gt_i32_e64 s[0:1], 0, v222
	s_waitcnt lgkmcnt(0)
	v_mfma_f32_16x16x32_bf16 v[16:19], v[8:11], v[16:19], 0
	v_mfma_f32_16x16x32_bf16 v[24:27], v[8:11], v[24:27], 0
	v_cndmask_b32_e32 v177, v249, v250, vcc
	v_cndmask_b32_e64 v186, v223, v224, s[0:1]
	v_max_u32_e32 v13, v13, v177
	v_min_u32_e32 v12, v12, v177
	v_max_u32_e32 v13, v13, v186
	v_min_u32_e32 v12, v12, v186
	ds_read_b128 v[248:251], v87 offset:49152
	ds_read_b128 v[222:225], v87 offset:50176
	v_max_f32_e32 v16, 0, v16
	v_max_f32_e32 v24, 0, v24
	v_max_f32_e32 v17, 0, v17
	v_max_f32_e32 v25, 0, v25
	v_max_f32_e32 v18, 0, v18
	v_max_f32_e32 v26, 0, v26
	v_max_f32_e32 v19, 0, v19
	v_max_f32_e32 v27, 0, v27
	v_pk_mul_f32 v[16:17], v[16:17], v[76:77]
	v_pk_mul_f32 v[24:25], v[24:25], v[76:77]
	v_mul_f32_e32 v18, v79, v18
	v_mul_f32_e32 v26, v79, v26
	v_mul_f32_e32 v19, v78, v19
	v_mul_f32_e32 v27, v78, v27
	v_add_f32_e32 v16, v16, v17
	v_add_f32_e32 v24, v24, v25
	v_add_f32_e32 v16, v18, v16
	v_add_f32_e32 v24, v26, v24
	v_add_f32_e32 v16, v19, v16
	v_add_f32_e32 v24, v27, v24
	v_add_f32_e32 v16, 0, v16
	v_add_f32_e32 v24, 0, v24
	v_min_u32_e32 v18, -2, v16
	v_min_u32_e32 v26, -2, v24
	v_or_b32_e32 v17, 0x80000000, v16
	v_or_b32_e32 v25, 0x80000000, v24
	v_not_b32_e32 v18, v18
	v_not_b32_e32 v26, v26
	v_cmp_gt_i32_e32 vcc, 0, v16
	v_cmp_gt_i32_e64 s[0:1], 0, v24
	s_waitcnt lgkmcnt(0)
	v_mfma_f32_16x16x32_bf16 v[248:251], v[8:11], v[248:251], 0
	v_mfma_f32_16x16x32_bf16 v[222:225], v[8:11], v[222:225], 0
	v_cndmask_b32_e32 v175, v17, v18, vcc
	v_cndmask_b32_e64 v184, v25, v26, s[0:1]
	v_max_u32_e32 v13, v13, v175
	v_min_u32_e32 v12, v12, v175
	v_max_u32_e32 v13, v13, v184
	v_min_u32_e32 v12, v12, v184
	s_cmp_eq_u64 s[26:27], 0
	s_cbranch_scc1 .Lmy_sel_zero_6
	ds_read_b128 v[16:19], v87 offset:51200
	ds_read_b128 v[24:27], v87 offset:52224
	v_max_f32_e32 v248, 0, v248
	v_max_f32_e32 v222, 0, v222
	v_max_f32_e32 v249, 0, v249
	v_max_f32_e32 v223, 0, v223
	v_max_f32_e32 v250, 0, v250
	v_max_f32_e32 v224, 0, v224
	v_max_f32_e32 v251, 0, v251
	v_max_f32_e32 v225, 0, v225
	v_pk_mul_f32 v[248:249], v[248:249], v[76:77]
	v_pk_mul_f32 v[222:223], v[222:223], v[76:77]
	v_mul_f32_e32 v250, v79, v250
	v_mul_f32_e32 v224, v79, v224
	v_mul_f32_e32 v251, v78, v251
	v_mul_f32_e32 v225, v78, v225
	v_add_f32_e32 v248, v248, v249
	v_add_f32_e32 v222, v222, v223
	v_add_f32_e32 v248, v250, v248
	v_add_f32_e32 v222, v224, v222
	v_add_f32_e32 v248, v251, v248
	v_add_f32_e32 v222, v225, v222
	v_add_f32_e32 v248, 0, v248
	v_add_f32_e32 v222, 0, v222
	v_min_u32_e32 v250, -2, v248
	v_min_u32_e32 v224, -2, v222
	v_or_b32_e32 v249, 0x80000000, v248
	v_or_b32_e32 v223, 0x80000000, v222
	v_not_b32_e32 v250, v250
	v_not_b32_e32 v224, v224
	v_cmp_gt_i32_e32 vcc, 0, v248
	v_cmp_gt_i32_e64 s[0:1], 0, v222
	s_waitcnt lgkmcnt(0)
	v_mfma_f32_16x16x32_bf16 v[16:19], v[8:11], v[16:19], 0
	v_mfma_f32_16x16x32_bf16 v[24:27], v[8:11], v[24:27], 0
	v_cndmask_b32_e32 v173, v249, v250, vcc
	v_cndmask_b32_e64 v182, v223, v224, s[0:1]
	v_max_u32_e32 v13, v13, v173
	v_min_u32_e32 v12, v12, v173
	v_max_u32_e32 v13, v13, v182
	v_min_u32_e32 v12, v12, v182
	ds_read_b128 v[248:251], v87 offset:53248
	ds_read_b128 v[222:225], v87 offset:54272
	v_max_f32_e32 v16, 0, v16
	v_max_f32_e32 v24, 0, v24
	v_max_f32_e32 v17, 0, v17
	v_max_f32_e32 v25, 0, v25
	v_max_f32_e32 v18, 0, v18
	v_max_f32_e32 v26, 0, v26
	v_max_f32_e32 v19, 0, v19
	v_max_f32_e32 v27, 0, v27
	v_pk_mul_f32 v[16:17], v[16:17], v[76:77]
	v_pk_mul_f32 v[24:25], v[24:25], v[76:77]
	v_mul_f32_e32 v18, v79, v18
	v_mul_f32_e32 v26, v79, v26
	v_mul_f32_e32 v19, v78, v19
	v_mul_f32_e32 v27, v78, v27
	v_add_f32_e32 v16, v16, v17
	v_add_f32_e32 v24, v24, v25
	v_add_f32_e32 v16, v18, v16
	v_add_f32_e32 v24, v26, v24
	v_add_f32_e32 v16, v19, v16
	v_add_f32_e32 v24, v27, v24
	v_add_f32_e32 v16, 0, v16
	v_add_f32_e32 v24, 0, v24
	v_min_u32_e32 v18, -2, v16
	v_min_u32_e32 v26, -2, v24
	v_or_b32_e32 v17, 0x80000000, v16
	v_or_b32_e32 v25, 0x80000000, v24
	v_not_b32_e32 v18, v18
	v_not_b32_e32 v26, v26
	v_cmp_gt_i32_e32 vcc, 0, v16
	v_cmp_gt_i32_e64 s[0:1], 0, v24
	s_waitcnt lgkmcnt(0)
	v_mfma_f32_16x16x32_bf16 v[248:251], v[8:11], v[248:251], 0
	v_mfma_f32_16x16x32_bf16 v[222:225], v[8:11], v[222:225], 0
	v_cndmask_b32_e32 v171, v17, v18, vcc
	v_cndmask_b32_e64 v180, v25, v26, s[0:1]
	v_max_u32_e32 v13, v13, v171
	v_min_u32_e32 v12, v12, v171
	v_max_u32_e32 v13, v13, v180
	v_min_u32_e32 v12, v12, v180
	ds_read_b128 v[16:19], v87 offset:55296
	ds_read_b128 v[24:27], v87 offset:56320
	v_max_f32_e32 v248, 0, v248
	v_max_f32_e32 v222, 0, v222
	v_max_f32_e32 v249, 0, v249
	v_max_f32_e32 v223, 0, v223
	v_max_f32_e32 v250, 0, v250
	v_max_f32_e32 v224, 0, v224
	v_max_f32_e32 v251, 0, v251
	v_max_f32_e32 v225, 0, v225
	v_pk_mul_f32 v[248:249], v[248:249], v[76:77]
	v_pk_mul_f32 v[222:223], v[222:223], v[76:77]
	v_mul_f32_e32 v250, v79, v250
	v_mul_f32_e32 v224, v79, v224
	v_mul_f32_e32 v251, v78, v251
	v_mul_f32_e32 v225, v78, v225
	v_add_f32_e32 v248, v248, v249
	v_add_f32_e32 v222, v222, v223
	v_add_f32_e32 v248, v250, v248
	v_add_f32_e32 v222, v224, v222
	v_add_f32_e32 v248, v251, v248
	v_add_f32_e32 v222, v225, v222
	v_add_f32_e32 v248, 0, v248
	v_add_f32_e32 v222, 0, v222
	v_min_u32_e32 v250, -2, v248
	v_min_u32_e32 v224, -2, v222
	v_or_b32_e32 v249, 0x80000000, v248
	v_or_b32_e32 v223, 0x80000000, v222
	v_not_b32_e32 v250, v250
	v_not_b32_e32 v224, v224
	v_cmp_gt_i32_e32 vcc, 0, v248
	v_cmp_gt_i32_e64 s[0:1], 0, v222
	s_waitcnt lgkmcnt(0)
	v_mfma_f32_16x16x32_bf16 v[16:19], v[8:11], v[16:19], 0
	v_mfma_f32_16x16x32_bf16 v[24:27], v[8:11], v[24:27], 0
	v_cndmask_b32_e32 v169, v249, v250, vcc
	v_cndmask_b32_e64 v178, v223, v224, s[0:1]
	v_max_u32_e32 v13, v13, v169
	v_min_u32_e32 v12, v12, v169
	v_max_u32_e32 v13, v13, v178
	v_min_u32_e32 v12, v12, v178
	ds_read_b128 v[248:251], v87 offset:57344
	ds_read_b128 v[222:225], v87 offset:58368
	v_max_f32_e32 v16, 0, v16
	v_max_f32_e32 v24, 0, v24
	v_max_f32_e32 v17, 0, v17
	v_max_f32_e32 v25, 0, v25
	v_max_f32_e32 v18, 0, v18
	v_max_f32_e32 v26, 0, v26
	v_max_f32_e32 v19, 0, v19
	v_max_f32_e32 v27, 0, v27
	v_pk_mul_f32 v[16:17], v[16:17], v[76:77]
	v_pk_mul_f32 v[24:25], v[24:25], v[76:77]
	v_mul_f32_e32 v18, v79, v18
	v_mul_f32_e32 v26, v79, v26
	v_mul_f32_e32 v19, v78, v19
	v_mul_f32_e32 v27, v78, v27
	v_add_f32_e32 v16, v16, v17
	v_add_f32_e32 v24, v24, v25
	v_add_f32_e32 v16, v18, v16
	v_add_f32_e32 v24, v26, v24
	v_add_f32_e32 v16, v19, v16
	v_add_f32_e32 v24, v27, v24
	v_add_f32_e32 v16, 0, v16
	v_add_f32_e32 v24, 0, v24
	v_min_u32_e32 v18, -2, v16
	v_min_u32_e32 v26, -2, v24
	v_or_b32_e32 v17, 0x80000000, v16
	v_or_b32_e32 v25, 0x80000000, v24
	v_not_b32_e32 v18, v18
	v_not_b32_e32 v26, v26
	v_cmp_gt_i32_e32 vcc, 0, v16
	v_cmp_gt_i32_e64 s[0:1], 0, v24
	s_waitcnt lgkmcnt(0)
	v_mfma_f32_16x16x32_bf16 v[248:251], v[8:11], v[248:251], 0
	v_mfma_f32_16x16x32_bf16 v[222:225], v[8:11], v[222:225], 0
	v_cndmask_b32_e32 v167, v17, v18, vcc
	v_cndmask_b32_e64 v176, v25, v26, s[0:1]
	v_max_u32_e32 v13, v13, v167
	v_min_u32_e32 v12, v12, v167
	v_max_u32_e32 v13, v13, v176
	v_min_u32_e32 v12, v12, v176
	s_cmp_eq_u64 s[10:11], 0
	s_cbranch_scc1 .Lmy_sel_zero_7
	ds_read_b128 v[16:19], v87 offset:59392
	ds_read_b128 v[24:27], v87 offset:60416
	v_max_f32_e32 v248, 0, v248
	v_max_f32_e32 v222, 0, v222
	v_max_f32_e32 v249, 0, v249
	v_max_f32_e32 v223, 0, v223
	v_max_f32_e32 v250, 0, v250
	v_max_f32_e32 v224, 0, v224
	v_max_f32_e32 v251, 0, v251
	v_max_f32_e32 v225, 0, v225
	v_pk_mul_f32 v[248:249], v[248:249], v[76:77]
	v_pk_mul_f32 v[222:223], v[222:223], v[76:77]
	v_mul_f32_e32 v250, v79, v250
	v_mul_f32_e32 v224, v79, v224
	v_mul_f32_e32 v251, v78, v251
	v_mul_f32_e32 v225, v78, v225
	v_add_f32_e32 v248, v248, v249
	v_add_f32_e32 v222, v222, v223
	v_add_f32_e32 v248, v250, v248
	v_add_f32_e32 v222, v224, v222
	v_add_f32_e32 v248, v251, v248
	v_add_f32_e32 v222, v225, v222
	v_add_f32_e32 v248, 0, v248
	v_add_f32_e32 v222, 0, v222
	v_min_u32_e32 v250, -2, v248
	v_min_u32_e32 v224, -2, v222
	v_or_b32_e32 v249, 0x80000000, v248
	v_or_b32_e32 v223, 0x80000000, v222
	v_not_b32_e32 v250, v250
	v_not_b32_e32 v224, v224
	v_cmp_gt_i32_e32 vcc, 0, v248
	v_cmp_gt_i32_e64 s[0:1], 0, v222
	s_waitcnt lgkmcnt(0)
	v_mfma_f32_16x16x32_bf16 v[16:19], v[8:11], v[16:19], 0
	v_mfma_f32_16x16x32_bf16 v[24:27], v[8:11], v[24:27], 0
	v_cndmask_b32_e32 v164, v249, v250, vcc
	v_cndmask_b32_e64 v174, v223, v224, s[0:1]
	v_max_u32_e32 v13, v13, v164
	v_min_u32_e32 v12, v12, v164
	v_max_u32_e32 v13, v13, v174
	v_min_u32_e32 v12, v12, v174
	ds_read_b128 v[248:251], v87 offset:61440
	ds_read_b128 v[222:225], v87 offset:62464
	v_max_f32_e32 v16, 0, v16
	v_max_f32_e32 v24, 0, v24
	v_max_f32_e32 v17, 0, v17
	v_max_f32_e32 v25, 0, v25
	v_max_f32_e32 v18, 0, v18
	v_max_f32_e32 v26, 0, v26
	v_max_f32_e32 v19, 0, v19
	v_max_f32_e32 v27, 0, v27
	v_pk_mul_f32 v[16:17], v[16:17], v[76:77]
	v_pk_mul_f32 v[24:25], v[24:25], v[76:77]
	v_mul_f32_e32 v18, v79, v18
	v_mul_f32_e32 v26, v79, v26
	v_mul_f32_e32 v19, v78, v19
	v_mul_f32_e32 v27, v78, v27
	v_add_f32_e32 v16, v16, v17
	v_add_f32_e32 v24, v24, v25
	v_add_f32_e32 v16, v18, v16
	v_add_f32_e32 v24, v26, v24
	v_add_f32_e32 v16, v19, v16
	v_add_f32_e32 v24, v27, v24
	v_add_f32_e32 v16, 0, v16
	v_add_f32_e32 v24, 0, v24
	v_min_u32_e32 v18, -2, v16
	v_min_u32_e32 v26, -2, v24
	v_or_b32_e32 v17, 0x80000000, v16
	v_or_b32_e32 v25, 0x80000000, v24
	v_not_b32_e32 v18, v18
	v_not_b32_e32 v26, v26
	v_cmp_gt_i32_e32 vcc, 0, v16
	v_cmp_gt_i32_e64 s[0:1], 0, v24
	s_waitcnt lgkmcnt(0)
	v_mfma_f32_16x16x32_bf16 v[248:251], v[8:11], v[248:251], 0
	v_mfma_f32_16x16x32_bf16 v[222:225], v[8:11], v[222:225], 0
	v_cndmask_b32_e32 v162, v17, v18, vcc
	v_cndmask_b32_e64 v172, v25, v26, s[0:1]
	v_max_u32_e32 v13, v13, v162
	v_min_u32_e32 v12, v12, v162
	v_max_u32_e32 v13, v13, v172
	v_min_u32_e32 v12, v12, v172
	ds_read_b128 v[16:19], v87 offset:63488
	ds_read_b128 v[24:27], v87 offset:64512
	v_max_f32_e32 v248, 0, v248
	v_max_f32_e32 v222, 0, v222
	v_max_f32_e32 v249, 0, v249
	v_max_f32_e32 v223, 0, v223
	v_max_f32_e32 v250, 0, v250
	v_max_f32_e32 v224, 0, v224
	v_max_f32_e32 v251, 0, v251
	v_max_f32_e32 v225, 0, v225
	v_pk_mul_f32 v[248:249], v[248:249], v[76:77]
	v_pk_mul_f32 v[222:223], v[222:223], v[76:77]
	v_mul_f32_e32 v250, v79, v250
	v_mul_f32_e32 v224, v79, v224
	v_mul_f32_e32 v251, v78, v251
	v_mul_f32_e32 v225, v78, v225
	v_add_f32_e32 v248, v248, v249
	v_add_f32_e32 v222, v222, v223
	v_add_f32_e32 v248, v250, v248
	v_add_f32_e32 v222, v224, v222
	v_add_f32_e32 v248, v251, v248
	v_add_f32_e32 v222, v225, v222
	v_add_f32_e32 v248, 0, v248
	v_add_f32_e32 v222, 0, v222
	v_min_u32_e32 v250, -2, v248
	v_min_u32_e32 v224, -2, v222
	v_or_b32_e32 v249, 0x80000000, v248
	v_or_b32_e32 v223, 0x80000000, v222
	v_not_b32_e32 v250, v250
	v_not_b32_e32 v224, v224
	v_cmp_gt_i32_e32 vcc, 0, v248
	v_cmp_gt_i32_e64 s[0:1], 0, v222
	s_waitcnt lgkmcnt(0)
	v_mfma_f32_16x16x32_bf16 v[16:19], v[8:11], v[16:19], 0
	v_mfma_f32_16x16x32_bf16 v[24:27], v[8:11], v[24:27], 0
	v_cndmask_b32_e32 v159, v249, v250, vcc
	v_cndmask_b32_e64 v170, v223, v224, s[0:1]
	v_max_u32_e32 v13, v13, v159
	v_min_u32_e32 v12, v12, v159
	v_max_u32_e32 v13, v13, v170
	v_min_u32_e32 v12, v12, v170
	ds_read_b128 v[248:251], v215
	ds_read_b128 v[222:225], v215 offset:1024
	v_max_f32_e32 v16, 0, v16
	v_max_f32_e32 v24, 0, v24
	v_max_f32_e32 v17, 0, v17
	v_max_f32_e32 v25, 0, v25
	v_max_f32_e32 v18, 0, v18
	v_max_f32_e32 v26, 0, v26
	v_max_f32_e32 v19, 0, v19
	v_max_f32_e32 v27, 0, v27
	v_pk_mul_f32 v[16:17], v[16:17], v[76:77]
	v_pk_mul_f32 v[24:25], v[24:25], v[76:77]
	v_mul_f32_e32 v18, v79, v18
	v_mul_f32_e32 v26, v79, v26
	v_mul_f32_e32 v19, v78, v19
	v_mul_f32_e32 v27, v78, v27
	v_add_f32_e32 v16, v16, v17
	v_add_f32_e32 v24, v24, v25
	v_add_f32_e32 v16, v18, v16
	v_add_f32_e32 v24, v26, v24
	v_add_f32_e32 v16, v19, v16
	v_add_f32_e32 v24, v27, v24
	v_add_f32_e32 v16, 0, v16
	v_add_f32_e32 v24, 0, v24
	v_min_u32_e32 v18, -2, v16
	v_min_u32_e32 v26, -2, v24
	v_or_b32_e32 v17, 0x80000000, v16
	v_or_b32_e32 v25, 0x80000000, v24
	v_not_b32_e32 v18, v18
	v_not_b32_e32 v26, v26
	v_cmp_gt_i32_e32 vcc, 0, v16
	v_cmp_gt_i32_e64 s[0:1], 0, v24
	s_waitcnt lgkmcnt(0)
	v_mfma_f32_16x16x32_bf16 v[248:251], v[8:11], v[248:251], 0
	v_mfma_f32_16x16x32_bf16 v[222:225], v[8:11], v[222:225], 0
	v_cndmask_b32_e32 v157, v17, v18, vcc
	v_cndmask_b32_e64 v168, v25, v26, s[0:1]
	v_max_u32_e32 v13, v13, v157
	v_min_u32_e32 v12, v12, v157
	v_max_u32_e32 v13, v13, v168
	v_min_u32_e32 v12, v12, v168
	s_cmp_eq_u64 s[28:29], 0
	s_cbranch_scc1 .Lmy_sel_zero_8
	ds_read_b128 v[16:19], v215 offset:2048
	ds_read_b128 v[24:27], v215 offset:3072
	v_max_f32_e32 v248, 0, v248
	v_max_f32_e32 v222, 0, v222
	v_max_f32_e32 v249, 0, v249
	v_max_f32_e32 v223, 0, v223
	v_max_f32_e32 v250, 0, v250
	v_max_f32_e32 v224, 0, v224
	v_max_f32_e32 v251, 0, v251
	v_max_f32_e32 v225, 0, v225
	v_pk_mul_f32 v[248:249], v[248:249], v[76:77]
	v_pk_mul_f32 v[222:223], v[222:223], v[76:77]
	v_mul_f32_e32 v250, v79, v250
	v_mul_f32_e32 v224, v79, v224
	v_mul_f32_e32 v251, v78, v251
	v_mul_f32_e32 v225, v78, v225
	v_add_f32_e32 v248, v248, v249
	v_add_f32_e32 v222, v222, v223
	v_add_f32_e32 v248, v250, v248
	v_add_f32_e32 v222, v224, v222
	v_add_f32_e32 v248, v251, v248
	v_add_f32_e32 v222, v225, v222
	v_add_f32_e32 v248, 0, v248
	v_add_f32_e32 v222, 0, v222
	v_min_u32_e32 v250, -2, v248
	v_min_u32_e32 v224, -2, v222
	v_or_b32_e32 v249, 0x80000000, v248
	v_or_b32_e32 v223, 0x80000000, v222
	v_not_b32_e32 v250, v250
	v_not_b32_e32 v224, v224
	v_cmp_gt_i32_e32 vcc, 0, v248
	v_cmp_gt_i32_e64 s[0:1], 0, v222
	s_waitcnt lgkmcnt(0)
	v_mfma_f32_16x16x32_bf16 v[16:19], v[8:11], v[16:19], 0
	v_mfma_f32_16x16x32_bf16 v[24:27], v[8:11], v[24:27], 0
	v_cndmask_b32_e32 v155, v249, v250, vcc
	v_cndmask_b32_e64 v166, v223, v224, s[0:1]
	v_max_u32_e32 v13, v13, v155
	v_min_u32_e32 v12, v12, v155
	v_max_u32_e32 v13, v13, v166
	v_min_u32_e32 v12, v12, v166
	ds_read_b128 v[248:251], v215 offset:4096
	ds_read_b128 v[222:225], v215 offset:5120
	v_max_f32_e32 v16, 0, v16
	v_max_f32_e32 v24, 0, v24
	v_max_f32_e32 v17, 0, v17
	v_max_f32_e32 v25, 0, v25
	v_max_f32_e32 v18, 0, v18
	v_max_f32_e32 v26, 0, v26
	v_max_f32_e32 v19, 0, v19
	v_max_f32_e32 v27, 0, v27
	v_pk_mul_f32 v[16:17], v[16:17], v[76:77]
	v_pk_mul_f32 v[24:25], v[24:25], v[76:77]
	v_mul_f32_e32 v18, v79, v18
	v_mul_f32_e32 v26, v79, v26
	v_mul_f32_e32 v19, v78, v19
	v_mul_f32_e32 v27, v78, v27
	v_add_f32_e32 v16, v16, v17
	v_add_f32_e32 v24, v24, v25
	v_add_f32_e32 v16, v18, v16
	v_add_f32_e32 v24, v26, v24
	v_add_f32_e32 v16, v19, v16
	v_add_f32_e32 v24, v27, v24
	v_add_f32_e32 v16, 0, v16
	v_add_f32_e32 v24, 0, v24
	v_min_u32_e32 v18, -2, v16
	v_min_u32_e32 v26, -2, v24
	v_or_b32_e32 v17, 0x80000000, v16
	v_or_b32_e32 v25, 0x80000000, v24
	v_not_b32_e32 v18, v18
	v_not_b32_e32 v26, v26
	v_cmp_gt_i32_e32 vcc, 0, v16
	v_cmp_gt_i32_e64 s[0:1], 0, v24
	s_waitcnt lgkmcnt(0)
	v_mfma_f32_16x16x32_bf16 v[248:251], v[8:11], v[248:251], 0
	v_mfma_f32_16x16x32_bf16 v[222:225], v[8:11], v[222:225], 0
	v_cndmask_b32_e32 v153, v17, v18, vcc
	v_cndmask_b32_e64 v165, v25, v26, s[0:1]
	v_max_u32_e32 v13, v13, v153
	v_min_u32_e32 v12, v12, v153
	v_max_u32_e32 v13, v13, v165
	v_min_u32_e32 v12, v12, v165
	ds_read_b128 v[16:19], v215 offset:6144
	ds_read_b128 v[24:27], v215 offset:7168
	v_max_f32_e32 v248, 0, v248
	v_max_f32_e32 v222, 0, v222
	v_max_f32_e32 v249, 0, v249
	v_max_f32_e32 v223, 0, v223
	v_max_f32_e32 v250, 0, v250
	v_max_f32_e32 v224, 0, v224
	v_max_f32_e32 v251, 0, v251
	v_max_f32_e32 v225, 0, v225
	v_pk_mul_f32 v[248:249], v[248:249], v[76:77]
	v_pk_mul_f32 v[222:223], v[222:223], v[76:77]
	v_mul_f32_e32 v250, v79, v250
	v_mul_f32_e32 v224, v79, v224
	v_mul_f32_e32 v251, v78, v251
	v_mul_f32_e32 v225, v78, v225
	v_add_f32_e32 v248, v248, v249
	v_add_f32_e32 v222, v222, v223
	v_add_f32_e32 v248, v250, v248
	v_add_f32_e32 v222, v224, v222
	v_add_f32_e32 v248, v251, v248
	v_add_f32_e32 v222, v225, v222
	v_add_f32_e32 v248, 0, v248
	v_add_f32_e32 v222, 0, v222
	v_min_u32_e32 v250, -2, v248
	v_min_u32_e32 v224, -2, v222
	v_or_b32_e32 v249, 0x80000000, v248
	v_or_b32_e32 v223, 0x80000000, v222
	v_not_b32_e32 v250, v250
	v_not_b32_e32 v224, v224
	v_cmp_gt_i32_e32 vcc, 0, v248
	v_cmp_gt_i32_e64 s[0:1], 0, v222
	s_waitcnt lgkmcnt(0)
	v_mfma_f32_16x16x32_bf16 v[16:19], v[8:11], v[16:19], 0
	v_mfma_f32_16x16x32_bf16 v[24:27], v[8:11], v[24:27], 0
	v_cndmask_b32_e32 v151, v249, v250, vcc
	v_cndmask_b32_e64 v163, v223, v224, s[0:1]
	v_max_u32_e32 v13, v13, v151
	v_min_u32_e32 v12, v12, v151
	v_max_u32_e32 v13, v13, v163
	v_min_u32_e32 v12, v12, v163
	ds_read_b128 v[248:251], v215 offset:8192
	ds_read_b128 v[222:225], v215 offset:9216
	v_max_f32_e32 v16, 0, v16
	v_max_f32_e32 v24, 0, v24
	v_max_f32_e32 v17, 0, v17
	v_max_f32_e32 v25, 0, v25
	v_max_f32_e32 v18, 0, v18
	v_max_f32_e32 v26, 0, v26
	v_max_f32_e32 v19, 0, v19
	v_max_f32_e32 v27, 0, v27
	v_pk_mul_f32 v[16:17], v[16:17], v[76:77]
	v_pk_mul_f32 v[24:25], v[24:25], v[76:77]
	v_mul_f32_e32 v18, v79, v18
	v_mul_f32_e32 v26, v79, v26
	v_mul_f32_e32 v19, v78, v19
	v_mul_f32_e32 v27, v78, v27
	v_add_f32_e32 v16, v16, v17
	v_add_f32_e32 v24, v24, v25
	v_add_f32_e32 v16, v18, v16
	v_add_f32_e32 v24, v26, v24
	v_add_f32_e32 v16, v19, v16
	v_add_f32_e32 v24, v27, v24
	v_add_f32_e32 v16, 0, v16
	v_add_f32_e32 v24, 0, v24
	v_min_u32_e32 v18, -2, v16
	v_min_u32_e32 v26, -2, v24
	v_or_b32_e32 v17, 0x80000000, v16
	v_or_b32_e32 v25, 0x80000000, v24
	v_not_b32_e32 v18, v18
	v_not_b32_e32 v26, v26
	v_cmp_gt_i32_e32 vcc, 0, v16
	v_cmp_gt_i32_e64 s[0:1], 0, v24
	s_waitcnt lgkmcnt(0)
	v_mfma_f32_16x16x32_bf16 v[248:251], v[8:11], v[248:251], 0
	v_mfma_f32_16x16x32_bf16 v[222:225], v[8:11], v[222:225], 0
	v_cndmask_b32_e32 v149, v17, v18, vcc
	v_cndmask_b32_e64 v160, v25, v26, s[0:1]
	v_max_u32_e32 v13, v13, v149
	v_min_u32_e32 v12, v12, v149
	v_max_u32_e32 v13, v13, v160
	v_min_u32_e32 v12, v12, v160
	s_cmp_eq_u64 s[30:31], 0
	s_cbranch_scc1 .Lmy_sel_zero_9
	ds_read_b128 v[16:19], v215 offset:10240
	ds_read_b128 v[24:27], v215 offset:11264
	v_max_f32_e32 v248, 0, v248
	v_max_f32_e32 v222, 0, v222
	v_max_f32_e32 v249, 0, v249
	v_max_f32_e32 v223, 0, v223
	v_max_f32_e32 v250, 0, v250
	v_max_f32_e32 v224, 0, v224
	v_max_f32_e32 v251, 0, v251
	v_max_f32_e32 v225, 0, v225
	v_pk_mul_f32 v[248:249], v[248:249], v[76:77]
	v_pk_mul_f32 v[222:223], v[222:223], v[76:77]
	v_mul_f32_e32 v250, v79, v250
	v_mul_f32_e32 v224, v79, v224
	v_mul_f32_e32 v251, v78, v251
	v_mul_f32_e32 v225, v78, v225
	v_add_f32_e32 v248, v248, v249
	v_add_f32_e32 v222, v222, v223
	v_add_f32_e32 v248, v250, v248
	v_add_f32_e32 v222, v224, v222
	v_add_f32_e32 v248, v251, v248
	v_add_f32_e32 v222, v225, v222
	v_add_f32_e32 v248, 0, v248
	v_add_f32_e32 v222, 0, v222
	v_min_u32_e32 v250, -2, v248
	v_min_u32_e32 v224, -2, v222
	v_or_b32_e32 v249, 0x80000000, v248
	v_or_b32_e32 v223, 0x80000000, v222
	v_not_b32_e32 v250, v250
	v_not_b32_e32 v224, v224
	v_cmp_gt_i32_e32 vcc, 0, v248
	v_cmp_gt_i32_e64 s[0:1], 0, v222
	s_waitcnt lgkmcnt(0)
	v_mfma_f32_16x16x32_bf16 v[16:19], v[8:11], v[16:19], 0
	v_mfma_f32_16x16x32_bf16 v[24:27], v[8:11], v[24:27], 0
	v_cndmask_b32_e32 v147, v249, v250, vcc
	v_cndmask_b32_e64 v158, v223, v224, s[0:1]
	v_max_u32_e32 v13, v13, v147
	v_min_u32_e32 v12, v12, v147
	v_max_u32_e32 v13, v13, v158
	v_min_u32_e32 v12, v12, v158
	ds_read_b128 v[248:251], v215 offset:12288
	ds_read_b128 v[222:225], v215 offset:13312
	v_max_f32_e32 v16, 0, v16
	v_max_f32_e32 v24, 0, v24
	v_max_f32_e32 v17, 0, v17
	v_max_f32_e32 v25, 0, v25
	v_max_f32_e32 v18, 0, v18
	v_max_f32_e32 v26, 0, v26
	v_max_f32_e32 v19, 0, v19
	v_max_f32_e32 v27, 0, v27
	v_pk_mul_f32 v[16:17], v[16:17], v[76:77]
	v_pk_mul_f32 v[24:25], v[24:25], v[76:77]
	v_mul_f32_e32 v18, v79, v18
	v_mul_f32_e32 v26, v79, v26
	v_mul_f32_e32 v19, v78, v19
	v_mul_f32_e32 v27, v78, v27
	v_add_f32_e32 v16, v16, v17
	v_add_f32_e32 v24, v24, v25
	v_add_f32_e32 v16, v18, v16
	v_add_f32_e32 v24, v26, v24
	v_add_f32_e32 v16, v19, v16
	v_add_f32_e32 v24, v27, v24
	v_add_f32_e32 v16, 0, v16
	v_add_f32_e32 v24, 0, v24
	v_min_u32_e32 v18, -2, v16
	v_min_u32_e32 v26, -2, v24
	v_or_b32_e32 v17, 0x80000000, v16
	v_or_b32_e32 v25, 0x80000000, v24
	v_not_b32_e32 v18, v18
	v_not_b32_e32 v26, v26
	v_cmp_gt_i32_e32 vcc, 0, v16
	v_cmp_gt_i32_e64 s[0:1], 0, v24
	s_waitcnt lgkmcnt(0)
	v_mfma_f32_16x16x32_bf16 v[248:251], v[8:11], v[248:251], 0
	v_mfma_f32_16x16x32_bf16 v[222:225], v[8:11], v[222:225], 0
	v_cndmask_b32_e32 v145, v17, v18, vcc
	v_cndmask_b32_e64 v156, v25, v26, s[0:1]
	v_max_u32_e32 v13, v13, v145
	v_min_u32_e32 v12, v12, v145
	v_max_u32_e32 v13, v13, v156
	v_min_u32_e32 v12, v12, v156
	ds_read_b128 v[16:19], v215 offset:14336
	ds_read_b128 v[24:27], v215 offset:15360
	v_max_f32_e32 v248, 0, v248
	v_max_f32_e32 v222, 0, v222
	v_max_f32_e32 v249, 0, v249
	v_max_f32_e32 v223, 0, v223
	v_max_f32_e32 v250, 0, v250
	v_max_f32_e32 v224, 0, v224
	v_max_f32_e32 v251, 0, v251
	v_max_f32_e32 v225, 0, v225
	v_pk_mul_f32 v[248:249], v[248:249], v[76:77]
	v_pk_mul_f32 v[222:223], v[222:223], v[76:77]
	v_mul_f32_e32 v250, v79, v250
	v_mul_f32_e32 v224, v79, v224
	v_mul_f32_e32 v251, v78, v251
	v_mul_f32_e32 v225, v78, v225
	v_add_f32_e32 v248, v248, v249
	v_add_f32_e32 v222, v222, v223
	v_add_f32_e32 v248, v250, v248
	v_add_f32_e32 v222, v224, v222
	v_add_f32_e32 v248, v251, v248
	v_add_f32_e32 v222, v225, v222
	v_add_f32_e32 v248, 0, v248
	v_add_f32_e32 v222, 0, v222
	v_min_u32_e32 v250, -2, v248
	v_min_u32_e32 v224, -2, v222
	v_or_b32_e32 v249, 0x80000000, v248
	v_or_b32_e32 v223, 0x80000000, v222
	v_not_b32_e32 v250, v250
	v_not_b32_e32 v224, v224
	v_cmp_gt_i32_e32 vcc, 0, v248
	v_cmp_gt_i32_e64 s[0:1], 0, v222
	s_waitcnt lgkmcnt(0)
	v_mfma_f32_16x16x32_bf16 v[16:19], v[8:11], v[16:19], 0
	v_mfma_f32_16x16x32_bf16 v[24:27], v[8:11], v[24:27], 0
	v_cndmask_b32_e32 v144, v249, v250, vcc
	v_cndmask_b32_e64 v154, v223, v224, s[0:1]
	v_max_u32_e32 v13, v13, v144
	v_min_u32_e32 v12, v12, v144
	v_max_u32_e32 v13, v13, v154
	v_min_u32_e32 v12, v12, v154
	ds_read_b128 v[248:251], v215 offset:16384
	ds_read_b128 v[222:225], v215 offset:17408
	v_max_f32_e32 v16, 0, v16
	v_max_f32_e32 v24, 0, v24
	v_max_f32_e32 v17, 0, v17
	v_max_f32_e32 v25, 0, v25
	v_max_f32_e32 v18, 0, v18
	v_max_f32_e32 v26, 0, v26
	v_max_f32_e32 v19, 0, v19
	v_max_f32_e32 v27, 0, v27
	v_pk_mul_f32 v[16:17], v[16:17], v[76:77]
	v_pk_mul_f32 v[24:25], v[24:25], v[76:77]
	v_mul_f32_e32 v18, v79, v18
	v_mul_f32_e32 v26, v79, v26
	v_mul_f32_e32 v19, v78, v19
	v_mul_f32_e32 v27, v78, v27
	v_add_f32_e32 v16, v16, v17
	v_add_f32_e32 v24, v24, v25
	v_add_f32_e32 v16, v18, v16
	v_add_f32_e32 v24, v26, v24
	v_add_f32_e32 v16, v19, v16
	v_add_f32_e32 v24, v27, v24
	v_add_f32_e32 v16, 0, v16
	v_add_f32_e32 v24, 0, v24
	v_min_u32_e32 v18, -2, v16
	v_min_u32_e32 v26, -2, v24
	v_or_b32_e32 v17, 0x80000000, v16
	v_or_b32_e32 v25, 0x80000000, v24
	v_not_b32_e32 v18, v18
	v_not_b32_e32 v26, v26
	v_cmp_gt_i32_e32 vcc, 0, v16
	v_cmp_gt_i32_e64 s[0:1], 0, v24
	s_waitcnt lgkmcnt(0)
	v_mfma_f32_16x16x32_bf16 v[248:251], v[8:11], v[248:251], 0
	v_mfma_f32_16x16x32_bf16 v[222:225], v[8:11], v[222:225], 0
	v_cndmask_b32_e32 v142, v17, v18, vcc
	v_cndmask_b32_e64 v152, v25, v26, s[0:1]
	v_max_u32_e32 v13, v13, v142
	v_min_u32_e32 v12, v12, v142
	v_max_u32_e32 v13, v13, v152
	v_min_u32_e32 v12, v12, v152
	s_cmp_eq_u64 s[34:35], 0
	s_cbranch_scc1 .Lmy_sel_zero_10
	ds_read_b128 v[16:19], v215 offset:18432
	ds_read_b128 v[24:27], v215 offset:19456
	v_max_f32_e32 v248, 0, v248
	v_max_f32_e32 v222, 0, v222
	v_max_f32_e32 v249, 0, v249
	v_max_f32_e32 v223, 0, v223
	v_max_f32_e32 v250, 0, v250
	v_max_f32_e32 v224, 0, v224
	v_max_f32_e32 v251, 0, v251
	v_max_f32_e32 v225, 0, v225
	v_pk_mul_f32 v[248:249], v[248:249], v[76:77]
	v_pk_mul_f32 v[222:223], v[222:223], v[76:77]
	v_mul_f32_e32 v250, v79, v250
	v_mul_f32_e32 v224, v79, v224
	v_mul_f32_e32 v251, v78, v251
	v_mul_f32_e32 v225, v78, v225
	v_add_f32_e32 v248, v248, v249
	v_add_f32_e32 v222, v222, v223
	v_add_f32_e32 v248, v250, v248
	v_add_f32_e32 v222, v224, v222
	v_add_f32_e32 v248, v251, v248
	v_add_f32_e32 v222, v225, v222
	v_add_f32_e32 v248, 0, v248
	v_add_f32_e32 v222, 0, v222
	v_min_u32_e32 v250, -2, v248
	v_min_u32_e32 v224, -2, v222
	v_or_b32_e32 v249, 0x80000000, v248
	v_or_b32_e32 v223, 0x80000000, v222
	v_not_b32_e32 v250, v250
	v_not_b32_e32 v224, v224
	v_cmp_gt_i32_e32 vcc, 0, v248
	v_cmp_gt_i32_e64 s[0:1], 0, v222
	s_waitcnt lgkmcnt(0)
	v_mfma_f32_16x16x32_bf16 v[16:19], v[8:11], v[16:19], 0
	v_mfma_f32_16x16x32_bf16 v[24:27], v[8:11], v[24:27], 0
	v_cndmask_b32_e32 v140, v249, v250, vcc
	v_cndmask_b32_e64 v150, v223, v224, s[0:1]
	v_max_u32_e32 v13, v13, v140
	v_min_u32_e32 v12, v12, v140
	v_max_u32_e32 v13, v13, v150
	v_min_u32_e32 v12, v12, v150
	ds_read_b128 v[248:251], v215 offset:20480
	ds_read_b128 v[222:225], v215 offset:21504
	v_max_f32_e32 v16, 0, v16
	v_max_f32_e32 v24, 0, v24
	v_max_f32_e32 v17, 0, v17
	v_max_f32_e32 v25, 0, v25
	v_max_f32_e32 v18, 0, v18
	v_max_f32_e32 v26, 0, v26
	v_max_f32_e32 v19, 0, v19
	v_max_f32_e32 v27, 0, v27
	v_pk_mul_f32 v[16:17], v[16:17], v[76:77]
	v_pk_mul_f32 v[24:25], v[24:25], v[76:77]
	v_mul_f32_e32 v18, v79, v18
	v_mul_f32_e32 v26, v79, v26
	v_mul_f32_e32 v19, v78, v19
	v_mul_f32_e32 v27, v78, v27
	v_add_f32_e32 v16, v16, v17
	v_add_f32_e32 v24, v24, v25
	v_add_f32_e32 v16, v18, v16
	v_add_f32_e32 v24, v26, v24
	v_add_f32_e32 v16, v19, v16
	v_add_f32_e32 v24, v27, v24
	v_add_f32_e32 v16, 0, v16
	v_add_f32_e32 v24, 0, v24
	v_min_u32_e32 v18, -2, v16
	v_min_u32_e32 v26, -2, v24
	v_or_b32_e32 v17, 0x80000000, v16
	v_or_b32_e32 v25, 0x80000000, v24
	v_not_b32_e32 v18, v18
	v_not_b32_e32 v26, v26
	v_cmp_gt_i32_e32 vcc, 0, v16
	v_cmp_gt_i32_e64 s[0:1], 0, v24
	s_waitcnt lgkmcnt(0)
	v_mfma_f32_16x16x32_bf16 v[248:251], v[8:11], v[248:251], 0
	v_mfma_f32_16x16x32_bf16 v[222:225], v[8:11], v[222:225], 0
	v_cndmask_b32_e32 v138, v17, v18, vcc
	v_cndmask_b32_e64 v148, v25, v26, s[0:1]
	v_max_u32_e32 v13, v13, v138
	v_min_u32_e32 v12, v12, v138
	v_max_u32_e32 v13, v13, v148
	v_min_u32_e32 v12, v12, v148
	ds_read_b128 v[16:19], v215 offset:22528
	ds_read_b128 v[24:27], v215 offset:23552
	v_max_f32_e32 v248, 0, v248
	v_max_f32_e32 v222, 0, v222
	v_max_f32_e32 v249, 0, v249
	v_max_f32_e32 v223, 0, v223
	v_max_f32_e32 v250, 0, v250
	v_max_f32_e32 v224, 0, v224
	v_max_f32_e32 v251, 0, v251
	v_max_f32_e32 v225, 0, v225
	v_pk_mul_f32 v[248:249], v[248:249], v[76:77]
	v_pk_mul_f32 v[222:223], v[222:223], v[76:77]
	v_mul_f32_e32 v250, v79, v250
	v_mul_f32_e32 v224, v79, v224
	v_mul_f32_e32 v251, v78, v251
	v_mul_f32_e32 v225, v78, v225
	v_add_f32_e32 v248, v248, v249
	v_add_f32_e32 v222, v222, v223
	v_add_f32_e32 v248, v250, v248
	v_add_f32_e32 v222, v224, v222
	v_add_f32_e32 v248, v251, v248
	v_add_f32_e32 v222, v225, v222
	v_add_f32_e32 v248, 0, v248
	v_add_f32_e32 v222, 0, v222
	v_min_u32_e32 v250, -2, v248
	v_min_u32_e32 v224, -2, v222
	v_or_b32_e32 v249, 0x80000000, v248
	v_or_b32_e32 v223, 0x80000000, v222
	v_not_b32_e32 v250, v250
	v_not_b32_e32 v224, v224
	v_cmp_gt_i32_e32 vcc, 0, v248
	v_cmp_gt_i32_e64 s[0:1], 0, v222
	s_waitcnt lgkmcnt(0)
	v_mfma_f32_16x16x32_bf16 v[16:19], v[8:11], v[16:19], 0
	v_mfma_f32_16x16x32_bf16 v[24:27], v[8:11], v[24:27], 0
	v_cndmask_b32_e32 v136, v249, v250, vcc
	v_cndmask_b32_e64 v146, v223, v224, s[0:1]
	v_max_u32_e32 v13, v13, v136
	v_min_u32_e32 v12, v12, v136
	v_max_u32_e32 v13, v13, v146
	v_min_u32_e32 v12, v12, v146
	ds_read_b128 v[248:251], v215 offset:24576
	ds_read_b128 v[222:225], v215 offset:25600
	v_max_f32_e32 v16, 0, v16
	v_max_f32_e32 v24, 0, v24
	v_max_f32_e32 v17, 0, v17
	v_max_f32_e32 v25, 0, v25
	v_max_f32_e32 v18, 0, v18
	v_max_f32_e32 v26, 0, v26
	v_max_f32_e32 v19, 0, v19
	v_max_f32_e32 v27, 0, v27
	v_pk_mul_f32 v[16:17], v[16:17], v[76:77]
	v_pk_mul_f32 v[24:25], v[24:25], v[76:77]
	v_mul_f32_e32 v18, v79, v18
	v_mul_f32_e32 v26, v79, v26
	v_mul_f32_e32 v19, v78, v19
	v_mul_f32_e32 v27, v78, v27
	v_add_f32_e32 v16, v16, v17
	v_add_f32_e32 v24, v24, v25
	v_add_f32_e32 v16, v18, v16
	v_add_f32_e32 v24, v26, v24
	v_add_f32_e32 v16, v19, v16
	v_add_f32_e32 v24, v27, v24
	v_add_f32_e32 v16, 0, v16
	v_add_f32_e32 v24, 0, v24
	v_min_u32_e32 v18, -2, v16
	v_min_u32_e32 v26, -2, v24
	v_or_b32_e32 v17, 0x80000000, v16
	v_or_b32_e32 v25, 0x80000000, v24
	v_not_b32_e32 v18, v18
	v_not_b32_e32 v26, v26
	v_cmp_gt_i32_e32 vcc, 0, v16
	v_cmp_gt_i32_e64 s[0:1], 0, v24
	s_waitcnt lgkmcnt(0)
	v_mfma_f32_16x16x32_bf16 v[248:251], v[8:11], v[248:251], 0
	v_mfma_f32_16x16x32_bf16 v[222:225], v[8:11], v[222:225], 0
	v_cndmask_b32_e32 v134, v17, v18, vcc
	v_cndmask_b32_e64 v143, v25, v26, s[0:1]
	v_max_u32_e32 v13, v13, v134
	v_min_u32_e32 v12, v12, v134
	v_max_u32_e32 v13, v13, v143
	v_min_u32_e32 v12, v12, v143
	s_cmp_eq_u64 s[12:13], 0
	s_cbranch_scc1 .Lmy_sel_zero_11
	ds_read_b128 v[16:19], v215 offset:26624
	ds_read_b128 v[24:27], v215 offset:27648
	v_max_f32_e32 v248, 0, v248
	v_max_f32_e32 v222, 0, v222
	v_max_f32_e32 v249, 0, v249
	v_max_f32_e32 v223, 0, v223
	v_max_f32_e32 v250, 0, v250
	v_max_f32_e32 v224, 0, v224
	v_max_f32_e32 v251, 0, v251
	v_max_f32_e32 v225, 0, v225
	v_pk_mul_f32 v[248:249], v[248:249], v[76:77]
	v_pk_mul_f32 v[222:223], v[222:223], v[76:77]
	v_mul_f32_e32 v250, v79, v250
	v_mul_f32_e32 v224, v79, v224
	v_mul_f32_e32 v251, v78, v251
	v_mul_f32_e32 v225, v78, v225
	v_add_f32_e32 v248, v248, v249
	v_add_f32_e32 v222, v222, v223
	v_add_f32_e32 v248, v250, v248
	v_add_f32_e32 v222, v224, v222
	v_add_f32_e32 v248, v251, v248
	v_add_f32_e32 v222, v225, v222
	v_add_f32_e32 v248, 0, v248
	v_add_f32_e32 v222, 0, v222
	v_min_u32_e32 v250, -2, v248
	v_min_u32_e32 v224, -2, v222
	v_or_b32_e32 v249, 0x80000000, v248
	v_or_b32_e32 v223, 0x80000000, v222
	v_not_b32_e32 v250, v250
	v_not_b32_e32 v224, v224
	v_cmp_gt_i32_e32 vcc, 0, v248
	v_cmp_gt_i32_e64 s[0:1], 0, v222
	s_waitcnt lgkmcnt(0)
	v_mfma_f32_16x16x32_bf16 v[16:19], v[8:11], v[16:19], 0
	v_mfma_f32_16x16x32_bf16 v[24:27], v[8:11], v[24:27], 0
	v_cndmask_b32_e32 v132, v249, v250, vcc
	v_cndmask_b32_e64 v141, v223, v224, s[0:1]
	v_max_u32_e32 v13, v13, v132
	v_min_u32_e32 v12, v12, v132
	v_max_u32_e32 v13, v13, v141
	v_min_u32_e32 v12, v12, v141
	ds_read_b128 v[248:251], v215 offset:28672
	ds_read_b128 v[222:225], v215 offset:29696
	v_max_f32_e32 v16, 0, v16
	v_max_f32_e32 v24, 0, v24
	v_max_f32_e32 v17, 0, v17
	v_max_f32_e32 v25, 0, v25
	v_max_f32_e32 v18, 0, v18
	v_max_f32_e32 v26, 0, v26
	v_max_f32_e32 v19, 0, v19
	v_max_f32_e32 v27, 0, v27
	v_pk_mul_f32 v[16:17], v[16:17], v[76:77]
	v_pk_mul_f32 v[24:25], v[24:25], v[76:77]
	v_mul_f32_e32 v18, v79, v18
	v_mul_f32_e32 v26, v79, v26
	v_mul_f32_e32 v19, v78, v19
	v_mul_f32_e32 v27, v78, v27
	v_add_f32_e32 v16, v16, v17
	v_add_f32_e32 v24, v24, v25
	v_add_f32_e32 v16, v18, v16
	v_add_f32_e32 v24, v26, v24
	v_add_f32_e32 v16, v19, v16
	v_add_f32_e32 v24, v27, v24
	v_add_f32_e32 v16, 0, v16
	v_add_f32_e32 v24, 0, v24
	v_min_u32_e32 v18, -2, v16
	v_min_u32_e32 v26, -2, v24
	v_or_b32_e32 v17, 0x80000000, v16
	v_or_b32_e32 v25, 0x80000000, v24
	v_not_b32_e32 v18, v18
	v_not_b32_e32 v26, v26
	v_cmp_gt_i32_e32 vcc, 0, v16
	v_cmp_gt_i32_e64 s[0:1], 0, v24
	s_waitcnt lgkmcnt(0)
	v_mfma_f32_16x16x32_bf16 v[248:251], v[8:11], v[248:251], 0
	v_mfma_f32_16x16x32_bf16 v[222:225], v[8:11], v[222:225], 0
	v_cndmask_b32_e32 v73, v17, v18, vcc
	v_cndmask_b32_e64 v139, v25, v26, s[0:1]
	v_max_u32_e32 v13, v13, v73
	v_min_u32_e32 v12, v12, v73
	v_max_u32_e32 v13, v13, v139
	v_min_u32_e32 v12, v12, v139
	ds_read_b128 v[16:19], v215 offset:30720
	ds_read_b128 v[24:27], v215 offset:31744
	v_max_f32_e32 v248, 0, v248
	v_max_f32_e32 v222, 0, v222
	v_max_f32_e32 v249, 0, v249
	v_max_f32_e32 v223, 0, v223
	v_max_f32_e32 v250, 0, v250
	v_max_f32_e32 v224, 0, v224
	v_max_f32_e32 v251, 0, v251
	v_max_f32_e32 v225, 0, v225
	v_pk_mul_f32 v[248:249], v[248:249], v[76:77]
	v_pk_mul_f32 v[222:223], v[222:223], v[76:77]
	v_mul_f32_e32 v250, v79, v250
	v_mul_f32_e32 v224, v79, v224
	v_mul_f32_e32 v251, v78, v251
	v_mul_f32_e32 v225, v78, v225
	v_add_f32_e32 v248, v248, v249
	v_add_f32_e32 v222, v222, v223
	v_add_f32_e32 v248, v250, v248
	v_add_f32_e32 v222, v224, v222
	v_add_f32_e32 v248, v251, v248
	v_add_f32_e32 v222, v225, v222
	v_add_f32_e32 v248, 0, v248
	v_add_f32_e32 v222, 0, v222
	v_min_u32_e32 v250, -2, v248
	v_min_u32_e32 v224, -2, v222
	v_or_b32_e32 v249, 0x80000000, v248
	v_or_b32_e32 v223, 0x80000000, v222
	v_not_b32_e32 v250, v250
	v_not_b32_e32 v224, v224
	v_cmp_gt_i32_e32 vcc, 0, v248
	v_cmp_gt_i32_e64 s[0:1], 0, v222
	s_waitcnt lgkmcnt(0)
	v_mfma_f32_16x16x32_bf16 v[16:19], v[8:11], v[16:19], 0
	v_mfma_f32_16x16x32_bf16 v[24:27], v[8:11], v[24:27], 0
	v_cndmask_b32_e32 v47, v249, v250, vcc
	v_cndmask_b32_e64 v137, v223, v224, s[0:1]
	v_max_u32_e32 v13, v13, v47
	v_min_u32_e32 v12, v12, v47
	v_max_u32_e32 v13, v13, v137
	v_min_u32_e32 v12, v12, v137
	ds_read_b128 v[248:251], v215 offset:32768
	ds_read_b128 v[222:225], v215 offset:33792
	v_max_f32_e32 v16, 0, v16
	v_max_f32_e32 v24, 0, v24
	v_max_f32_e32 v17, 0, v17
	v_max_f32_e32 v25, 0, v25
	v_max_f32_e32 v18, 0, v18
	v_max_f32_e32 v26, 0, v26
	v_max_f32_e32 v19, 0, v19
	v_max_f32_e32 v27, 0, v27
	v_pk_mul_f32 v[16:17], v[16:17], v[76:77]
	v_pk_mul_f32 v[24:25], v[24:25], v[76:77]
	v_mul_f32_e32 v18, v79, v18
	v_mul_f32_e32 v26, v79, v26
	v_mul_f32_e32 v19, v78, v19
	v_mul_f32_e32 v27, v78, v27
	v_add_f32_e32 v16, v16, v17
	v_add_f32_e32 v24, v24, v25
	v_add_f32_e32 v16, v18, v16
	v_add_f32_e32 v24, v26, v24
	v_add_f32_e32 v16, v19, v16
	v_add_f32_e32 v24, v27, v24
	v_add_f32_e32 v16, 0, v16
	v_add_f32_e32 v24, 0, v24
	v_min_u32_e32 v18, -2, v16
	v_min_u32_e32 v26, -2, v24
	v_or_b32_e32 v17, 0x80000000, v16
	v_or_b32_e32 v25, 0x80000000, v24
	v_not_b32_e32 v18, v18
	v_not_b32_e32 v26, v26
	v_cmp_gt_i32_e32 vcc, 0, v16
	v_cmp_gt_i32_e64 s[0:1], 0, v24
	s_waitcnt lgkmcnt(0)
	v_mfma_f32_16x16x32_bf16 v[248:251], v[8:11], v[248:251], 0
	v_mfma_f32_16x16x32_bf16 v[222:225], v[8:11], v[222:225], 0
	v_cndmask_b32_e32 v42, v17, v18, vcc
	v_cndmask_b32_e64 v135, v25, v26, s[0:1]
	v_max_u32_e32 v13, v13, v42
	v_min_u32_e32 v12, v12, v42
	v_max_u32_e32 v13, v13, v135
	v_min_u32_e32 v12, v12, v135
	s_cmp_eq_u64 s[36:37], 0
	s_cbranch_scc1 .Lmy_sel_zero_12
	ds_read_b128 v[16:19], v215 offset:34816
	ds_read_b128 v[24:27], v215 offset:35840
	v_max_f32_e32 v248, 0, v248
	v_max_f32_e32 v222, 0, v222
	v_max_f32_e32 v249, 0, v249
	v_max_f32_e32 v223, 0, v223
	v_max_f32_e32 v250, 0, v250
	v_max_f32_e32 v224, 0, v224
	v_max_f32_e32 v251, 0, v251
	v_max_f32_e32 v225, 0, v225
	v_pk_mul_f32 v[248:249], v[248:249], v[76:77]
	v_pk_mul_f32 v[222:223], v[222:223], v[76:77]
	v_mul_f32_e32 v250, v79, v250
	v_mul_f32_e32 v224, v79, v224
	v_mul_f32_e32 v251, v78, v251
	v_mul_f32_e32 v225, v78, v225
	v_add_f32_e32 v248, v248, v249
	v_add_f32_e32 v222, v222, v223
	v_add_f32_e32 v248, v250, v248
	v_add_f32_e32 v222, v224, v222
	v_add_f32_e32 v248, v251, v248
	v_add_f32_e32 v222, v225, v222
	v_add_f32_e32 v248, 0, v248
	v_add_f32_e32 v222, 0, v222
	v_min_u32_e32 v250, -2, v248
	v_min_u32_e32 v224, -2, v222
	v_or_b32_e32 v249, 0x80000000, v248
	v_or_b32_e32 v223, 0x80000000, v222
	v_not_b32_e32 v250, v250
	v_not_b32_e32 v224, v224
	v_cmp_gt_i32_e32 vcc, 0, v248
	v_cmp_gt_i32_e64 s[0:1], 0, v222
	s_waitcnt lgkmcnt(0)
	v_mfma_f32_16x16x32_bf16 v[16:19], v[8:11], v[16:19], 0
	v_mfma_f32_16x16x32_bf16 v[24:27], v[8:11], v[24:27], 0
	v_cndmask_b32_e32 v40, v249, v250, vcc
	v_cndmask_b32_e64 v133, v223, v224, s[0:1]
	v_max_u32_e32 v13, v13, v40
	v_min_u32_e32 v12, v12, v40
	v_max_u32_e32 v13, v13, v133
	v_min_u32_e32 v12, v12, v133
	ds_read_b128 v[248:251], v215 offset:36864
	ds_read_b128 v[222:225], v215 offset:37888
	v_max_f32_e32 v16, 0, v16
	v_max_f32_e32 v24, 0, v24
	v_max_f32_e32 v17, 0, v17
	v_max_f32_e32 v25, 0, v25
	v_max_f32_e32 v18, 0, v18
	v_max_f32_e32 v26, 0, v26
	v_max_f32_e32 v19, 0, v19
	v_max_f32_e32 v27, 0, v27
	v_pk_mul_f32 v[16:17], v[16:17], v[76:77]
	v_pk_mul_f32 v[24:25], v[24:25], v[76:77]
	v_mul_f32_e32 v18, v79, v18
	v_mul_f32_e32 v26, v79, v26
	v_mul_f32_e32 v19, v78, v19
	v_mul_f32_e32 v27, v78, v27
	v_add_f32_e32 v16, v16, v17
	v_add_f32_e32 v24, v24, v25
	v_add_f32_e32 v16, v18, v16
	v_add_f32_e32 v24, v26, v24
	v_add_f32_e32 v16, v19, v16
	v_add_f32_e32 v24, v27, v24
	v_add_f32_e32 v16, 0, v16
	v_add_f32_e32 v24, 0, v24
	v_min_u32_e32 v18, -2, v16
	v_min_u32_e32 v26, -2, v24
	v_or_b32_e32 v17, 0x80000000, v16
	v_or_b32_e32 v25, 0x80000000, v24
	v_not_b32_e32 v18, v18
	v_not_b32_e32 v26, v26
	v_cmp_gt_i32_e32 vcc, 0, v16
	v_cmp_gt_i32_e64 s[0:1], 0, v24
	s_waitcnt lgkmcnt(0)
	v_mfma_f32_16x16x32_bf16 v[248:251], v[8:11], v[248:251], 0
	v_mfma_f32_16x16x32_bf16 v[222:225], v[8:11], v[222:225], 0
	v_cndmask_b32_e32 v38, v17, v18, vcc
	v_cndmask_b32_e64 v75, v25, v26, s[0:1]
	v_max_u32_e32 v13, v13, v38
	v_min_u32_e32 v12, v12, v38
	v_max_u32_e32 v13, v13, v75
	v_min_u32_e32 v12, v12, v75
	ds_read_b128 v[16:19], v215 offset:38912
	ds_read_b128 v[24:27], v215 offset:39936
	v_max_f32_e32 v248, 0, v248
	v_max_f32_e32 v222, 0, v222
	v_max_f32_e32 v249, 0, v249
	v_max_f32_e32 v223, 0, v223
	v_max_f32_e32 v250, 0, v250
	v_max_f32_e32 v224, 0, v224
	v_max_f32_e32 v251, 0, v251
	v_max_f32_e32 v225, 0, v225
	v_pk_mul_f32 v[248:249], v[248:249], v[76:77]
	v_pk_mul_f32 v[222:223], v[222:223], v[76:77]
	v_mul_f32_e32 v250, v79, v250
	v_mul_f32_e32 v224, v79, v224
	v_mul_f32_e32 v251, v78, v251
	v_mul_f32_e32 v225, v78, v225
	v_add_f32_e32 v248, v248, v249
	v_add_f32_e32 v222, v222, v223
	v_add_f32_e32 v248, v250, v248
	v_add_f32_e32 v222, v224, v222
	v_add_f32_e32 v248, v251, v248
	v_add_f32_e32 v222, v225, v222
	v_add_f32_e32 v248, 0, v248
	v_add_f32_e32 v222, 0, v222
	v_min_u32_e32 v250, -2, v248
	v_min_u32_e32 v224, -2, v222
	v_or_b32_e32 v249, 0x80000000, v248
	v_or_b32_e32 v223, 0x80000000, v222
	v_not_b32_e32 v250, v250
	v_not_b32_e32 v224, v224
	v_cmp_gt_i32_e32 vcc, 0, v248
	v_cmp_gt_i32_e64 s[0:1], 0, v222
	s_waitcnt lgkmcnt(0)
	v_mfma_f32_16x16x32_bf16 v[16:19], v[8:11], v[16:19], 0
	v_mfma_f32_16x16x32_bf16 v[24:27], v[8:11], v[24:27], 0
	v_cndmask_b32_e32 v34, v249, v250, vcc
	v_cndmask_b32_e64 v67, v223, v224, s[0:1]
	v_max_u32_e32 v13, v13, v34
	v_min_u32_e32 v12, v12, v34
	v_max_u32_e32 v13, v13, v67
	v_min_u32_e32 v12, v12, v67
	s_nop 1
	v_max_f32_e32 v16, 0, v16
	v_max_f32_e32 v24, 0, v24
	v_max_f32_e32 v17, 0, v17
	v_max_f32_e32 v25, 0, v25
	v_max_f32_e32 v18, 0, v18
	v_max_f32_e32 v26, 0, v26
	v_max_f32_e32 v19, 0, v19
	v_max_f32_e32 v27, 0, v27
	v_pk_mul_f32 v[16:17], v[16:17], v[76:77]
	v_pk_mul_f32 v[24:25], v[24:25], v[76:77]
	v_mul_f32_e32 v18, v79, v18
	v_mul_f32_e32 v26, v79, v26
	v_mul_f32_e32 v19, v78, v19
	v_mul_f32_e32 v27, v78, v27
	v_add_f32_e32 v16, v16, v17
	v_add_f32_e32 v24, v24, v25
	v_add_f32_e32 v16, v18, v16
	v_add_f32_e32 v24, v26, v24
	v_add_f32_e32 v16, v19, v16
	v_add_f32_e32 v24, v27, v24
	v_add_f32_e32 v16, 0, v16
	v_add_f32_e32 v24, 0, v24
	v_min_u32_e32 v18, -2, v16
	v_min_u32_e32 v26, -2, v24
	v_or_b32_e32 v17, 0x80000000, v16
	v_or_b32_e32 v25, 0x80000000, v24
	v_not_b32_e32 v18, v18
	v_not_b32_e32 v26, v26
	v_cmp_gt_i32_e32 vcc, 0, v16
	v_cmp_gt_i32_e64 s[0:1], 0, v24
	s_nop 1
	v_cndmask_b32_e32 v32, v17, v18, vcc
	v_cndmask_b32_e64 v43, v25, v26, s[0:1]
	v_max_u32_e32 v13, v13, v32
	v_min_u32_e32 v12, v12, v32
	v_max_u32_e32 v13, v13, v43
	v_min_u32_e32 v12, v12, v43
	s_cmp_eq_u64 s[38:39], 0
	s_cbranch_scc1 .Lmy_sel_zero_13
	ds_read_b128 v[248:251], v215 offset:40960
	ds_read_b128 v[222:225], v215 offset:41984
	s_waitcnt lgkmcnt(0)
	v_mfma_f32_16x16x32_bf16 v[248:251], v[8:11], v[248:251], 0
	v_mfma_f32_16x16x32_bf16 v[222:225], v[8:11], v[222:225], 0
	s_nop 6
	v_max_f32_e32 v248, 0, v248
	v_max_f32_e32 v222, 0, v222
	v_max_f32_e32 v249, 0, v249
	v_max_f32_e32 v223, 0, v223
	v_max_f32_e32 v250, 0, v250
	v_max_f32_e32 v224, 0, v224
	v_max_f32_e32 v251, 0, v251
	v_max_f32_e32 v225, 0, v225
	v_pk_mul_f32 v[248:249], v[248:249], v[76:77]
	v_pk_mul_f32 v[222:223], v[222:223], v[76:77]
	v_mul_f32_e32 v250, v79, v250
	v_mul_f32_e32 v224, v79, v224
	v_mul_f32_e32 v251, v78, v251
	v_mul_f32_e32 v225, v78, v225
	v_add_f32_e32 v248, v248, v249
	v_add_f32_e32 v222, v222, v223
	v_add_f32_e32 v248, v250, v248
	v_add_f32_e32 v222, v224, v222
	v_add_f32_e32 v248, v251, v248
	v_add_f32_e32 v222, v225, v222
	v_add_f32_e32 v248, 0, v248
	v_add_f32_e32 v222, 0, v222
	v_min_u32_e32 v250, -2, v248
	v_min_u32_e32 v224, -2, v222
	v_or_b32_e32 v249, 0x80000000, v248
	v_or_b32_e32 v223, 0x80000000, v222
	v_not_b32_e32 v250, v250
	v_not_b32_e32 v224, v224
	v_cmp_gt_i32_e32 vcc, 0, v248
	v_cmp_gt_i32_e64 s[0:1], 0, v222
	s_nop 1
	v_cndmask_b32_e32 v30, v249, v250, vcc
	v_cndmask_b32_e64 v41, v223, v224, s[0:1]
	v_max_u32_e32 v13, v13, v30
	v_min_u32_e32 v12, v12, v30
	v_max_u32_e32 v13, v13, v41
	v_min_u32_e32 v12, v12, v41
	ds_read_b128 v[248:251], v215 offset:43008
	ds_read_b128 v[222:225], v215 offset:44032
	s_waitcnt lgkmcnt(0)
	v_mfma_f32_16x16x32_bf16 v[248:251], v[8:11], v[248:251], 0
	v_mfma_f32_16x16x32_bf16 v[222:225], v[8:11], v[222:225], 0
	s_nop 6
	v_max_f32_e32 v248, 0, v248
	v_max_f32_e32 v222, 0, v222
	v_max_f32_e32 v249, 0, v249
	v_max_f32_e32 v223, 0, v223
	v_max_f32_e32 v250, 0, v250
	v_max_f32_e32 v224, 0, v224
	v_max_f32_e32 v251, 0, v251
	v_max_f32_e32 v225, 0, v225
	v_pk_mul_f32 v[248:249], v[248:249], v[76:77]
	v_pk_mul_f32 v[222:223], v[222:223], v[76:77]
	v_mul_f32_e32 v250, v79, v250
	v_mul_f32_e32 v224, v79, v224
	v_mul_f32_e32 v251, v78, v251
	v_mul_f32_e32 v225, v78, v225
	v_add_f32_e32 v248, v248, v249
	v_add_f32_e32 v222, v222, v223
	v_add_f32_e32 v248, v250, v248
	v_add_f32_e32 v222, v224, v222
	v_add_f32_e32 v248, v251, v248
	v_add_f32_e32 v222, v225, v222
	v_add_f32_e32 v248, 0, v248
	v_add_f32_e32 v222, 0, v222
	v_min_u32_e32 v250, -2, v248
	v_min_u32_e32 v224, -2, v222
	v_or_b32_e32 v249, 0x80000000, v248
	v_or_b32_e32 v223, 0x80000000, v222
	v_not_b32_e32 v250, v250
	v_not_b32_e32 v224, v224
	v_cmp_gt_i32_e32 vcc, 0, v248
	v_cmp_gt_i32_e64 s[0:1], 0, v222
	s_nop 1
	v_cndmask_b32_e32 v26, v249, v250, vcc
	v_cndmask_b32_e64 v39, v223, v224, s[0:1]
	v_max_u32_e32 v13, v13, v26
	v_min_u32_e32 v12, v12, v26
	v_max_u32_e32 v13, v13, v39
	v_min_u32_e32 v12, v12, v39
	ds_read_b128 v[248:251], v215 offset:45056
	ds_read_b128 v[222:225], v215 offset:46080
	s_waitcnt lgkmcnt(0)
	v_mfma_f32_16x16x32_bf16 v[248:251], v[8:11], v[248:251], 0
	v_mfma_f32_16x16x32_bf16 v[222:225], v[8:11], v[222:225], 0
	s_nop 6
	v_max_f32_e32 v248, 0, v248
	v_max_f32_e32 v222, 0, v222
	v_max_f32_e32 v249, 0, v249
	v_max_f32_e32 v223, 0, v223
	v_max_f32_e32 v250, 0, v250
	v_max_f32_e32 v224, 0, v224
	v_max_f32_e32 v251, 0, v251
	v_max_f32_e32 v225, 0, v225
	v_pk_mul_f32 v[248:249], v[248:249], v[76:77]
	v_pk_mul_f32 v[222:223], v[222:223], v[76:77]
	v_mul_f32_e32 v250, v79, v250
	v_mul_f32_e32 v224, v79, v224
	v_mul_f32_e32 v251, v78, v251
	v_mul_f32_e32 v225, v78, v225
	v_add_f32_e32 v248, v248, v249
	v_add_f32_e32 v222, v222, v223
	v_add_f32_e32 v248, v250, v248
	v_add_f32_e32 v222, v224, v222
	v_add_f32_e32 v248, v251, v248
	v_add_f32_e32 v222, v225, v222
	v_add_f32_e32 v248, 0, v248
	v_add_f32_e32 v222, 0, v222
	v_min_u32_e32 v250, -2, v248
	v_min_u32_e32 v224, -2, v222
	v_or_b32_e32 v249, 0x80000000, v248
	v_or_b32_e32 v223, 0x80000000, v222
	v_not_b32_e32 v250, v250
	v_not_b32_e32 v224, v224
	v_cmp_gt_i32_e32 vcc, 0, v248
	v_cmp_gt_i32_e64 s[0:1], 0, v222
	s_nop 1
	v_cndmask_b32_e32 v24, v249, v250, vcc
	v_cndmask_b32_e64 v35, v223, v224, s[0:1]
	v_max_u32_e32 v13, v13, v24
	v_min_u32_e32 v12, v12, v24
	v_max_u32_e32 v13, v13, v35
	v_min_u32_e32 v12, v12, v35
	ds_read_b128 v[248:251], v215 offset:47104
	ds_read_b128 v[222:225], v215 offset:48128
	s_waitcnt lgkmcnt(0)
	v_mfma_f32_16x16x32_bf16 v[248:251], v[8:11], v[248:251], 0
	v_mfma_f32_16x16x32_bf16 v[222:225], v[8:11], v[222:225], 0
	s_nop 6
	v_max_f32_e32 v248, 0, v248
	v_max_f32_e32 v222, 0, v222
	v_max_f32_e32 v249, 0, v249
	v_max_f32_e32 v223, 0, v223
	v_max_f32_e32 v250, 0, v250
	v_max_f32_e32 v224, 0, v224
	v_max_f32_e32 v251, 0, v251
	v_max_f32_e32 v225, 0, v225
	v_pk_mul_f32 v[248:249], v[248:249], v[76:77]
	v_pk_mul_f32 v[222:223], v[222:223], v[76:77]
	v_mul_f32_e32 v250, v79, v250
	v_mul_f32_e32 v224, v79, v224
	v_mul_f32_e32 v251, v78, v251
	v_mul_f32_e32 v225, v78, v225
	v_add_f32_e32 v248, v248, v249
	v_add_f32_e32 v222, v222, v223
	v_add_f32_e32 v248, v250, v248
	v_add_f32_e32 v222, v224, v222
	v_add_f32_e32 v248, v251, v248
	v_add_f32_e32 v222, v225, v222
	v_add_f32_e32 v248, 0, v248
	v_add_f32_e32 v222, 0, v222
	v_min_u32_e32 v250, -2, v248
	v_min_u32_e32 v224, -2, v222
	v_or_b32_e32 v249, 0x80000000, v248
	v_or_b32_e32 v223, 0x80000000, v222
	v_not_b32_e32 v250, v250
	v_not_b32_e32 v224, v224
	v_cmp_gt_i32_e32 vcc, 0, v248
	v_cmp_gt_i32_e64 s[0:1], 0, v222
	s_nop 1
	v_cndmask_b32_e32 v22, v249, v250, vcc
	v_cndmask_b32_e64 v33, v223, v224, s[0:1]
	v_max_u32_e32 v13, v13, v22
	v_min_u32_e32 v12, v12, v22
	v_max_u32_e32 v13, v13, v33
	v_min_u32_e32 v12, v12, v33
	s_cmp_eq_u64 s[40:41], 0
	s_cbranch_scc1 .Lmy_sel_zero_14
	ds_read_b128 v[248:251], v215 offset:49152
	ds_read_b128 v[222:225], v215 offset:50176
	s_waitcnt lgkmcnt(0)
	v_mfma_f32_16x16x32_bf16 v[248:251], v[8:11], v[248:251], 0
	v_mfma_f32_16x16x32_bf16 v[222:225], v[8:11], v[222:225], 0
	s_nop 6
	v_max_f32_e32 v248, 0, v248
	v_max_f32_e32 v222, 0, v222
	v_max_f32_e32 v249, 0, v249
	v_max_f32_e32 v223, 0, v223
	v_max_f32_e32 v250, 0, v250
	v_max_f32_e32 v224, 0, v224
	v_max_f32_e32 v251, 0, v251
	v_max_f32_e32 v225, 0, v225
	v_pk_mul_f32 v[248:249], v[248:249], v[76:77]
	v_pk_mul_f32 v[222:223], v[222:223], v[76:77]
	v_mul_f32_e32 v250, v79, v250
	v_mul_f32_e32 v224, v79, v224
	v_mul_f32_e32 v251, v78, v251
	v_mul_f32_e32 v225, v78, v225
	v_add_f32_e32 v248, v248, v249
	v_add_f32_e32 v222, v222, v223
	v_add_f32_e32 v248, v250, v248
	v_add_f32_e32 v222, v224, v222
	v_add_f32_e32 v248, v251, v248
	v_add_f32_e32 v222, v225, v222
	v_add_f32_e32 v248, 0, v248
	v_add_f32_e32 v222, 0, v222
	v_min_u32_e32 v250, -2, v248
	v_min_u32_e32 v224, -2, v222
	v_or_b32_e32 v249, 0x80000000, v248
	v_or_b32_e32 v223, 0x80000000, v222
	v_not_b32_e32 v250, v250
	v_not_b32_e32 v224, v224
	v_cmp_gt_i32_e32 vcc, 0, v248
	v_cmp_gt_i32_e64 s[0:1], 0, v222
	s_nop 1
	v_cndmask_b32_e32 v19, v249, v250, vcc
	v_cndmask_b32_e64 v31, v223, v224, s[0:1]
	v_max_u32_e32 v13, v13, v19
	v_min_u32_e32 v12, v12, v19
	v_max_u32_e32 v13, v13, v31
	v_min_u32_e32 v12, v12, v31
	ds_read_b128 v[248:251], v215 offset:51200
	ds_read_b128 v[222:225], v215 offset:52224
	s_waitcnt lgkmcnt(0)
	v_mfma_f32_16x16x32_bf16 v[248:251], v[8:11], v[248:251], 0
	v_mfma_f32_16x16x32_bf16 v[222:225], v[8:11], v[222:225], 0
	s_nop 6
	v_max_f32_e32 v248, 0, v248
	v_max_f32_e32 v222, 0, v222
	v_max_f32_e32 v249, 0, v249
	v_max_f32_e32 v223, 0, v223
	v_max_f32_e32 v250, 0, v250
	v_max_f32_e32 v224, 0, v224
	v_max_f32_e32 v251, 0, v251
	v_max_f32_e32 v225, 0, v225
	v_pk_mul_f32 v[248:249], v[248:249], v[76:77]
	v_pk_mul_f32 v[222:223], v[222:223], v[76:77]
	v_mul_f32_e32 v250, v79, v250
	v_mul_f32_e32 v224, v79, v224
	v_mul_f32_e32 v251, v78, v251
	v_mul_f32_e32 v225, v78, v225
	v_add_f32_e32 v248, v248, v249
	v_add_f32_e32 v222, v222, v223
	v_add_f32_e32 v248, v250, v248
	v_add_f32_e32 v222, v224, v222
	v_add_f32_e32 v248, v251, v248
	v_add_f32_e32 v222, v225, v222
	v_add_f32_e32 v248, 0, v248
	v_add_f32_e32 v222, 0, v222
	v_min_u32_e32 v250, -2, v248
	v_min_u32_e32 v224, -2, v222
	v_or_b32_e32 v249, 0x80000000, v248
	v_or_b32_e32 v223, 0x80000000, v222
	v_not_b32_e32 v250, v250
	v_not_b32_e32 v224, v224
	v_cmp_gt_i32_e32 vcc, 0, v248
	v_cmp_gt_i32_e64 s[0:1], 0, v222
	s_nop 1
	v_cndmask_b32_e32 v18, v249, v250, vcc
	v_cndmask_b32_e64 v27, v223, v224, s[0:1]
	v_max_u32_e32 v13, v13, v18
	v_min_u32_e32 v12, v12, v18
	v_max_u32_e32 v13, v13, v27
	v_min_u32_e32 v12, v12, v27
	ds_read_b128 v[248:251], v215 offset:53248
	ds_read_b128 v[222:225], v215 offset:54272
	s_waitcnt lgkmcnt(0)
	v_mfma_f32_16x16x32_bf16 v[248:251], v[8:11], v[248:251], 0
	v_mfma_f32_16x16x32_bf16 v[222:225], v[8:11], v[222:225], 0
	s_nop 6
	v_max_f32_e32 v248, 0, v248
	v_max_f32_e32 v222, 0, v222
	v_max_f32_e32 v249, 0, v249
	v_max_f32_e32 v223, 0, v223
	v_max_f32_e32 v250, 0, v250
	v_max_f32_e32 v224, 0, v224
	v_max_f32_e32 v251, 0, v251
	v_max_f32_e32 v225, 0, v225
	v_pk_mul_f32 v[248:249], v[248:249], v[76:77]
	v_pk_mul_f32 v[222:223], v[222:223], v[76:77]
	v_mul_f32_e32 v250, v79, v250
	v_mul_f32_e32 v224, v79, v224
	v_mul_f32_e32 v251, v78, v251
	v_mul_f32_e32 v225, v78, v225
	v_add_f32_e32 v248, v248, v249
	v_add_f32_e32 v222, v222, v223
	v_add_f32_e32 v248, v250, v248
	v_add_f32_e32 v222, v224, v222
	v_add_f32_e32 v248, v251, v248
	v_add_f32_e32 v222, v225, v222
	v_add_f32_e32 v248, 0, v248
	v_add_f32_e32 v222, 0, v222
	v_min_u32_e32 v250, -2, v248
	v_min_u32_e32 v224, -2, v222
	v_or_b32_e32 v249, 0x80000000, v248
	v_or_b32_e32 v223, 0x80000000, v222
	v_not_b32_e32 v250, v250
	v_not_b32_e32 v224, v224
	v_cmp_gt_i32_e32 vcc, 0, v248
	v_cmp_gt_i32_e64 s[0:1], 0, v222
	s_nop 1
	v_cndmask_b32_e32 v17, v249, v250, vcc
	v_cndmask_b32_e64 v25, v223, v224, s[0:1]
	v_max_u32_e32 v13, v13, v17
	v_min_u32_e32 v12, v12, v17
	v_max_u32_e32 v13, v13, v25
	v_min_u32_e32 v12, v12, v25
	ds_read_b128 v[248:251], v215 offset:55296
	ds_read_b128 v[222:225], v215 offset:56320
	s_waitcnt lgkmcnt(0)
	v_mfma_f32_16x16x32_bf16 v[248:251], v[8:11], v[248:251], 0
	v_mfma_f32_16x16x32_bf16 v[222:225], v[8:11], v[222:225], 0
	s_nop 6
	v_max_f32_e32 v248, 0, v248
	v_max_f32_e32 v222, 0, v222
	v_max_f32_e32 v249, 0, v249
	v_max_f32_e32 v223, 0, v223
	v_max_f32_e32 v250, 0, v250
	v_max_f32_e32 v224, 0, v224
	v_max_f32_e32 v251, 0, v251
	v_max_f32_e32 v225, 0, v225
	v_pk_mul_f32 v[248:249], v[248:249], v[76:77]
	v_pk_mul_f32 v[222:223], v[222:223], v[76:77]
	v_mul_f32_e32 v250, v79, v250
	v_mul_f32_e32 v224, v79, v224
	v_mul_f32_e32 v251, v78, v251
	v_mul_f32_e32 v225, v78, v225
	v_add_f32_e32 v248, v248, v249
	v_add_f32_e32 v222, v222, v223
	v_add_f32_e32 v248, v250, v248
	v_add_f32_e32 v222, v224, v222
	v_add_f32_e32 v248, v251, v248
	v_add_f32_e32 v222, v225, v222
	v_add_f32_e32 v248, 0, v248
	v_add_f32_e32 v222, 0, v222
	v_min_u32_e32 v250, -2, v248
	v_min_u32_e32 v224, -2, v222
	v_or_b32_e32 v249, 0x80000000, v248
	v_or_b32_e32 v223, 0x80000000, v222
	v_not_b32_e32 v250, v250
	v_not_b32_e32 v224, v224
	v_cmp_gt_i32_e32 vcc, 0, v248
	v_cmp_gt_i32_e64 s[0:1], 0, v222
	s_nop 1
	v_cndmask_b32_e32 v16, v249, v250, vcc
	v_cndmask_b32_e64 v23, v223, v224, s[0:1]
	v_max_u32_e32 v13, v13, v16
	v_min_u32_e32 v12, v12, v16
	v_max_u32_e32 v13, v13, v23
	v_min_u32_e32 v12, v12, v23
	s_branch .Lmy_sel_done
.Lmy_sel_zero_0:
	v_mov_b32_e32 v247, 0
	v_mov_b32_e32 v246, 0
	v_mov_b32_e32 v210, 0
	v_mov_b32_e32 v245, 0
	v_mov_b32_e32 v239, 0
	v_mov_b32_e32 v244, 0
	v_mov_b32_e32 v237, 0
	v_mov_b32_e32 v243, 0
.Lmy_sel_zero_1:
	v_mov_b32_e32 v235, 0
	v_mov_b32_e32 v242, 0
	v_mov_b32_e32 v212, 0
	v_mov_b32_e32 v241, 0
	v_mov_b32_e32 v209, 0
	v_mov_b32_e32 v240, 0
	v_mov_b32_e32 v207, 0
	v_mov_b32_e32 v238, 0
.Lmy_sel_zero_2:
	v_mov_b32_e32 v205, 0
	v_mov_b32_e32 v236, 0
	v_mov_b32_e32 v203, 0
	v_mov_b32_e32 v213, 0
	v_mov_b32_e32 v201, 0
	v_mov_b32_e32 v211, 0
	v_mov_b32_e32 v199, 0
	v_mov_b32_e32 v208, 0
.Lmy_sel_zero_3:
	v_mov_b32_e32 v197, 0
	v_mov_b32_e32 v206, 0
	v_mov_b32_e32 v195, 0
	v_mov_b32_e32 v204, 0
	v_mov_b32_e32 v193, 0
	v_mov_b32_e32 v202, 0
	v_mov_b32_e32 v191, 0
	v_mov_b32_e32 v200, 0
.Lmy_sel_zero_4:
	v_mov_b32_e32 v189, 0
	v_mov_b32_e32 v198, 0
	v_mov_b32_e32 v187, 0
	v_mov_b32_e32 v196, 0
	v_mov_b32_e32 v185, 0
	v_mov_b32_e32 v194, 0
	v_mov_b32_e32 v183, 0
	v_mov_b32_e32 v192, 0
.Lmy_sel_zero_5:
	v_mov_b32_e32 v181, 0
	v_mov_b32_e32 v190, 0
	v_mov_b32_e32 v179, 0
	v_mov_b32_e32 v188, 0
	v_mov_b32_e32 v177, 0
	v_mov_b32_e32 v186, 0
	v_mov_b32_e32 v175, 0
	v_mov_b32_e32 v184, 0
.Lmy_sel_zero_6:
	v_mov_b32_e32 v173, 0
	v_mov_b32_e32 v182, 0
	v_mov_b32_e32 v171, 0
	v_mov_b32_e32 v180, 0
	v_mov_b32_e32 v169, 0
	v_mov_b32_e32 v178, 0
	v_mov_b32_e32 v167, 0
	v_mov_b32_e32 v176, 0
.Lmy_sel_zero_7:
	v_mov_b32_e32 v164, 0
	v_mov_b32_e32 v174, 0
	v_mov_b32_e32 v162, 0
	v_mov_b32_e32 v172, 0
	v_mov_b32_e32 v159, 0
	v_mov_b32_e32 v170, 0
	v_mov_b32_e32 v157, 0
	v_mov_b32_e32 v168, 0
.Lmy_sel_zero_8:
	v_mov_b32_e32 v155, 0
	v_mov_b32_e32 v166, 0
	v_mov_b32_e32 v153, 0
	v_mov_b32_e32 v165, 0
	v_mov_b32_e32 v151, 0
	v_mov_b32_e32 v163, 0
	v_mov_b32_e32 v149, 0
	v_mov_b32_e32 v160, 0
.Lmy_sel_zero_9:
	v_mov_b32_e32 v147, 0
	v_mov_b32_e32 v158, 0
	v_mov_b32_e32 v145, 0
	v_mov_b32_e32 v156, 0
	v_mov_b32_e32 v144, 0
	v_mov_b32_e32 v154, 0
	v_mov_b32_e32 v142, 0
	v_mov_b32_e32 v152, 0
.Lmy_sel_zero_10:
	v_mov_b32_e32 v140, 0
	v_mov_b32_e32 v150, 0
	v_mov_b32_e32 v138, 0
	v_mov_b32_e32 v148, 0
	v_mov_b32_e32 v136, 0
	v_mov_b32_e32 v146, 0
	v_mov_b32_e32 v134, 0
	v_mov_b32_e32 v143, 0
.Lmy_sel_zero_11:
	v_mov_b32_e32 v132, 0
	v_mov_b32_e32 v141, 0
	v_mov_b32_e32 v73, 0
	v_mov_b32_e32 v139, 0
	v_mov_b32_e32 v47, 0
	v_mov_b32_e32 v137, 0
	v_mov_b32_e32 v42, 0
	v_mov_b32_e32 v135, 0
.Lmy_sel_zero_12:
	v_mov_b32_e32 v40, 0
	v_mov_b32_e32 v133, 0
	v_mov_b32_e32 v38, 0
	v_mov_b32_e32 v75, 0
	v_mov_b32_e32 v34, 0
	v_mov_b32_e32 v67, 0
	v_mov_b32_e32 v32, 0
	v_mov_b32_e32 v43, 0
.Lmy_sel_zero_13:
	v_mov_b32_e32 v30, 0
	v_mov_b32_e32 v41, 0
	v_mov_b32_e32 v26, 0
	v_mov_b32_e32 v39, 0
	v_mov_b32_e32 v24, 0
	v_mov_b32_e32 v35, 0
	v_mov_b32_e32 v22, 0
	v_mov_b32_e32 v33, 0
.Lmy_sel_zero_14:
	v_mov_b32_e32 v19, 0
	v_mov_b32_e32 v31, 0
	v_mov_b32_e32 v18, 0
	v_mov_b32_e32 v27, 0
	v_mov_b32_e32 v17, 0
	v_mov_b32_e32 v25, 0
	v_mov_b32_e32 v16, 0
	v_mov_b32_e32 v23, 0
.Lmy_sel_done:
.LBB0_826:
	v_or_b32_e32 v8, 3, v74
	s_movk_i32 s0, 0xff
	v_cmp_lt_i32_e32 vcc, s0, v8
	s_mov_b64 s[62:63], 0
	v_bfrev_b32_e32 v9, -2
	v_mov_b32_e32 v8, 1
	s_and_saveexec_b64 s[64:65], vcc
	s_cbranch_execz .LBB0_873
	v_and_b32_e32 v8, 64, v214
	v_add_u32_e32 v8, 64, v8
	v_xor_b32_e32 v9, 1, v214
	v_cmp_lt_i32_e32 vcc, v9, v8
	v_xor_b32_e32 v11, 2, v214
	s_movk_i32 s0, 0x100
	v_cndmask_b32_e32 v9, v214, v9, vcc
	v_lshlrev_b32_e32 v74, 2, v9
	ds_bpermute_b32 v9, v74, v13
	v_cmp_lt_i32_e32 vcc, v11, v8
	ds_bpermute_b32 v10, v74, v12
	s_mov_b32 s50, 0
	v_cndmask_b32_e32 v11, v214, v11, vcc
	s_waitcnt lgkmcnt(1)
	v_max_u32_e32 v9, v13, v9
	v_lshlrev_b32_e32 v76, 2, v11
	ds_bpermute_b32 v11, v76, v9
	s_waitcnt lgkmcnt(1)
	v_min_u32_e32 v10, v12, v10
	v_mov_b32_e32 v79, 0x437f8000
	v_mov_b32_e32 v248, 0
	s_waitcnt lgkmcnt(0)
	v_max_u32_e32 v9, v9, v11
	ds_bpermute_b32 v11, v76, v10
	s_waitcnt lgkmcnt(0)
	v_min_u32_e32 v10, v10, v11
	v_xor_b32_e32 v11, 4, v214
	v_cmp_lt_i32_e32 vcc, v11, v8
	s_nop 1
	v_cndmask_b32_e32 v11, v214, v11, vcc
	v_lshlrev_b32_e32 v77, 2, v11
	ds_bpermute_b32 v11, v77, v9
	s_waitcnt lgkmcnt(0)
	v_max_u32_e32 v9, v9, v11
	ds_bpermute_b32 v11, v77, v10
	s_waitcnt lgkmcnt(0)
	v_min_u32_e32 v10, v10, v11
	v_xor_b32_e32 v11, 8, v214
	v_cmp_lt_i32_e32 vcc, v11, v8
	s_nop 1
	v_cndmask_b32_e32 v8, v214, v11, vcc
	v_lshlrev_b32_e32 v78, 2, v8
	ds_bpermute_b32 v8, v78, v9
	v_cmp_gt_i32_e32 vcc, s0, v72
	s_movk_i32 s0, 0xff
	v_cmp_lt_i32_e64 s[0:1], s0, v72
	s_waitcnt lgkmcnt(0)
	v_max_u32_e32 v8, v9, v8
	ds_bpermute_b32 v9, v78, v10
	v_add_u32_e32 v8, 1, v8
	v_cndmask_b32_e64 v8, 2, v8, s[0:1]
	s_waitcnt lgkmcnt(0)
	v_min_u32_e32 v9, v10, v9
	v_cndmask_b32_e64 v9, 1, v9, s[0:1]
	v_cmp_gt_u32_e64 s[2:3], v8, v9
	v_add_u32_e32 v10, 1, v9
	s_nop 0
	v_cndmask_b32_e64 v8, v10, v8, s[2:3]
	v_add_u32_e32 v10, 1, v72
	v_cvt_f32_i32_e32 v10, v10
	v_add_f32_e32 v72, 0xc37f8000, v10
	v_sub_u32_e32 v10, v8, v9
	v_cmp_eq_u32_e64 s[2:3], 1, v10
	s_or_b64 s[2:3], s[2:3], vcc
